# B: MoE-up first-unit row-index loads issued together (one wait); C: trailing half's post-epilogue barrier moved to just before the next unit's K-loop in MoE up/down
# baseline (speedup 1.0000x reference)
;     __device__ __forceinline__ bool next(int i, pg8::Unit& u) const { if (i > 0) return false; u.pm = pm; u.pn = pn; u.e = 0; u.mt = 0; u.cnt = 0; u.lx = 0; u.a = A + ((size_t)pm * 256 + rowoff) * 2048; u.b = Bt + (size_t)pn * 256 * 2048; return true; }
; template <class Epi, class Sched, bool ALIGN_EPI = false, bool SP2 = false, bool GATHER = false, bool HALFM = false>
; __device__ __forceinline__ void gemm_phase(PG8_LAS unsigned char* lds, const int Kdim, const Sched& S, const Epi& E) {
;     ...
;     if constexpr (GATHER) { static_assert(SP2, "GATHER needs the SP2 loop"); gA = S.abase();
;         Unit u1; const bool h1 = S.next(1, u1);
; #pragma unroll
;         for (int h = 0; h < 2; ++h)
; #pragma unroll
;             for (int i = 0; i < 2; ++i) { gc[h][i] = (unsigned)S.row_index(cur, h * HALF + RA[i]) * (unsigned)(K * 2) + CA2[i]; gn[h][i] = h1 ? (unsigned)S.row_index(u1, h * HALF + RA[i]) * (unsigned)(K * 2) + CA2[i] : gc[h][i]; } }
.LBB0_1670:
	v_ashrrev_i32_e32 v1, 31, v2
	v_lshrrev_b32_e32 v1, 26, v1
	v_add_u32_e32 v1, v2, v1
	v_ashrrev_i32_e32 v6, 6, v1
	v_bfe_i32 v1, v2, 27, 1
	v_lshlrev_b32_e32 v5, 4, v2
	v_lshrrev_b32_e32 v1, 22, v1
	v_add_u32_e32 v1, v5, v1
	v_and_b32_e32 v1, 0xfffffc00, v1
	v_sub_u32_e32 v1, v5, v1
	v_lshrrev_b32_e32 v4, 4, v1
	v_bitop3_b32 v7, v4, v1, 32 bitop3:0x6c
	v_ashrrev_i32_e32 v1, 31, v1
	v_lshrrev_b32_e32 v1, 26, v1
	v_lshlrev_b32_e32 v4, 3, v6
	v_add_u32_e32 v1, v7, v1
	v_and_b32_e32 v8, -16, v4
	v_ashrrev_i32_e32 v4, 6, v1
	v_add_u32_e32 v1, v4, v8
	v_add_u32_e32 v9, s7, v1
	s_mul_i32 s15, s46, 0x4800
	v_cmp_gt_i32_e32 vcc, s8, v9
	v_mov_b32_e32 v148, 0
	s_and_saveexec_b64 s[4:5], vcc
	v_readlane_b32 s20, v255, 8
	v_readlane_b32 s21, v255, 9
	s_cbranch_execz .LBB0_1672
	v_add_u32_e32 v8, s15, v9
	v_readlane_b32 s16, v251, 3
	v_ashrrev_i32_e32 v9, 31, v8
	v_readlane_b32 s17, v251, 4
	s_nop 1
	v_lshl_add_u64 v[8:9], v[8:9], 2, s[16:17]
	global_load_dword v148, v[8:9], off
.LBB0_1672:
	s_or_b64 exec, exec, s[4:5]
	v_mul_i32_i24_e32 v9, 64, v4
	v_sub_u32_e32 v7, v7, v9
	v_lshlrev_b32_e32 v6, 5, v6
	v_ashrrev_i16_sdwa v7, v212, sext(v7) dst_sel:DWORD dst_unused:UNUSED_PAD src0_sel:DWORD src1_sel:BYTE_0
	v_and_b32_e32 v6, 32, v6
	v_bfe_i32 v7, v7, 0, 16
	v_add_lshl_u32 v162, v6, v7, 1
	v_cndmask_b32_e64 v6, 0, 1, s[0:1]
	v_cmp_ne_u32_e64 s[42:43], 1, v6
	s_andn2_b64 vcc, exec, s[0:1]
	s_cbranch_vccnz .LBB0_1676
	v_add_u32_e32 v7, s13, v1
	v_cmp_gt_i32_e32 vcc, s14, v7
	v_mov_b32_e32 v163, 0
	s_and_saveexec_b64 s[0:1], vcc
	s_cbranch_execz .LBB0_1675
	v_add_u32_e32 v6, s12, v7
	v_readlane_b32 s4, v251, 3
	v_ashrrev_i32_e32 v7, 31, v6
	v_readlane_b32 s5, v251, 4
	s_nop 1
	v_lshl_add_u64 v[6:7], v[6:7], 2, s[4:5]
	global_load_dword v163, v[6:7], off

;     __device__ __forceinline__ bool next(int i, pg8::Unit& u) const { if (i > 0) return false; u.pm = pm; u.pn = pn; u.e = 0; u.mt = 0; u.cnt = 0; u.lx = 0; u.a = A + ((size_t)pm * 256 + rowoff) * 2048; u.b = Bt + (size_t)pn * 256 * 2048; return true; }
; template <class Epi, class Sched, bool ALIGN_EPI = false, bool SP2 = false, bool GATHER = false, bool HALFM = false>
; __device__ __forceinline__ void gemm_phase(PG8_LAS unsigned char* lds, const int Kdim, const Sched& S, const Epi& E) {
;     ...
;     if constexpr (GATHER) { static_assert(SP2, "GATHER needs the SP2 loop"); gA = S.abase();
;         Unit u1; const bool h1 = S.next(1, u1);
; #pragma unroll
;         for (int h = 0; h < 2; ++h)
; #pragma unroll
;             for (int i = 0; i < 2; ++i) { gc[h][i] = (unsigned)S.row_index(cur, h * HALF + RA[i]) * (unsigned)(K * 2) + CA2[i]; gn[h][i] = h1 ? (unsigned)S.row_index(u1, h * HALF + RA[i]) * (unsigned)(K * 2) + CA2[i] : gc[h][i]; } }
.LBB0_1676:
	v_add_u32_e32 v5, 0x2000, v5
	v_ashrrev_i32_e32 v6, 31, v5
	v_lshrrev_b32_e32 v6, 22, v6
	v_add_u32_e32 v6, v5, v6
	v_ashrrev_i32_e32 v6, 10, v6
	v_mul_i32_i24_e32 v7, 0x400, v6
	v_sub_u32_e32 v5, v5, v7
	v_lshrrev_b32_e32 v7, 4, v5
	v_bitop3_b32 v7, v7, v5, 32 bitop3:0x6c
	v_lshlrev_b32_e32 v5, 3, v6
	v_and_b32_e32 v8, -16, v5
	v_ashrrev_i32_e32 v5, 31, v7
	v_lshrrev_b32_e32 v5, 26, v5
	v_add_u32_e32 v5, v7, v5
	v_ashrrev_i32_e32 v5, 6, v5
	v_add_u32_e32 v164, v5, v8
	v_add_u32_e32 v9, s7, v164
	v_cmp_gt_i32_e32 vcc, s8, v9
	v_mov_b32_e32 v150, 0
	s_and_saveexec_b64 s[0:1], vcc
	s_cbranch_execz .LBB0_1678
	v_add_u32_e32 v8, s15, v9
	v_readlane_b32 s4, v251, 3
	v_ashrrev_i32_e32 v9, 31, v8
	v_readlane_b32 s5, v251, 4
	s_nop 1
	v_lshl_add_u64 v[8:9], v[8:9], 2, s[4:5]
	global_load_dword v150, v[8:9], off
.LBB0_1678:
	s_or_b64 exec, exec, s[0:1]
	v_lshlrev_b32_e32 v9, 6, v5
	v_sub_u32_e32 v7, v7, v9
	v_lshlrev_b32_e32 v6, 5, v6
	v_ashrrev_i16_sdwa v7, v212, sext(v7) dst_sel:DWORD dst_unused:UNUSED_PAD src0_sel:DWORD src1_sel:BYTE_0
	v_and_b32_e32 v6, 32, v6
	v_bfe_i32 v7, v7, 0, 16
	v_add_lshl_u32 v165, v6, v7, 1
	s_and_b64 vcc, exec, s[42:43]
	s_cbranch_vccnz .LBB0_1682
	v_add_u32_e32 v7, s13, v164
	v_cmp_gt_i32_e32 vcc, s14, v7
	v_mov_b32_e32 v166, 0
	s_and_saveexec_b64 s[0:1], vcc
	s_cbranch_execz .LBB0_1681
	v_add_u32_e32 v6, s12, v7
	v_readlane_b32 s4, v251, 3
	v_ashrrev_i32_e32 v7, 31, v6
	v_readlane_b32 s5, v251, 4
	s_nop 1
	v_lshl_add_u64 v[6:7], v[6:7], 2, s[4:5]
	global_load_dword v166, v[6:7], off

;     __device__ __forceinline__ bool next(int i, pg8::Unit& u) const { if (i > 0) return false; u.pm = pm; u.pn = pn; u.e = 0; u.mt = 0; u.cnt = 0; u.lx = 0; u.a = A + ((size_t)pm * 256 + rowoff) * 2048; u.b = Bt + (size_t)pn * 256 * 2048; return true; }
; template <class Epi, class Sched, bool ALIGN_EPI = false, bool SP2 = false, bool GATHER = false, bool HALFM = false>
; __device__ __forceinline__ void gemm_phase(PG8_LAS unsigned char* lds, const int Kdim, const Sched& S, const Epi& E) {
;     ...
;     if constexpr (GATHER) { static_assert(SP2, "GATHER needs the SP2 loop"); gA = S.abase();
;         Unit u1; const bool h1 = S.next(1, u1);
; #pragma unroll
;         for (int h = 0; h < 2; ++h)
; #pragma unroll
;             for (int i = 0; i < 2; ++i) { gc[h][i] = (unsigned)S.row_index(cur, h * HALF + RA[i]) * (unsigned)(K * 2) + CA2[i]; gn[h][i] = h1 ? (unsigned)S.row_index(u1, h * HALF + RA[i]) * (unsigned)(K * 2) + CA2[i] : gc[h][i]; } }
.LBB0_1682:
	v_add_u32_e32 v6, 0x80, v1
	v_add_u32_e32 v8, s7, v6
	v_cmp_gt_i32_e32 vcc, s8, v8
	v_mov_b32_e32 v152, 0
	s_and_saveexec_b64 s[0:1], vcc
	s_cbranch_execz .LBB0_1684
	v_add_u32_e32 v8, s15, v8
	v_readlane_b32 s4, v251, 3
	v_ashrrev_i32_e32 v9, 31, v8
	v_readlane_b32 s5, v251, 4
	s_nop 1
	v_lshl_add_u64 v[8:9], v[8:9], 2, s[4:5]
	global_load_dword v152, v[8:9], off
.LBB0_1684:
	s_or_b64 exec, exec, s[0:1]
	s_and_b64 vcc, exec, s[42:43]
	s_cbranch_vccnz .LBB0_1688
	v_add_u32_e32 v7, s13, v6
	v_cmp_gt_i32_e32 vcc, s14, v7
	v_mov_b32_e32 v167, 0
	s_and_saveexec_b64 s[0:1], vcc
	s_cbranch_execz .LBB0_1687
	v_add_u32_e32 v6, s12, v7
	v_readlane_b32 s4, v251, 3
	v_ashrrev_i32_e32 v7, 31, v6
	v_readlane_b32 s5, v251, 4
	s_nop 1
	v_lshl_add_u64 v[6:7], v[6:7], 2, s[4:5]
	global_load_dword v167, v[6:7], off

;     __device__ __forceinline__ bool next(int i, pg8::Unit& u) const { if (i > 0) return false; u.pm = pm; u.pn = pn; u.e = 0; u.mt = 0; u.cnt = 0; u.lx = 0; u.a = A + ((size_t)pm * 256 + rowoff) * 2048; u.b = Bt + (size_t)pn * 256 * 2048; return true; }
; template <class Epi, class Sched, bool ALIGN_EPI = false, bool SP2 = false, bool GATHER = false, bool HALFM = false>
; __device__ __forceinline__ void gemm_phase(PG8_LAS unsigned char* lds, const int Kdim, const Sched& S, const Epi& E) {
;     ...
;     if constexpr (GATHER) { static_assert(SP2, "GATHER needs the SP2 loop"); gA = S.abase();
;         Unit u1; const bool h1 = S.next(1, u1);
; #pragma unroll
;         for (int h = 0; h < 2; ++h)
; #pragma unroll
;             for (int i = 0; i < 2; ++i) { gc[h][i] = (unsigned)S.row_index(cur, h * HALF + RA[i]) * (unsigned)(K * 2) + CA2[i]; gn[h][i] = h1 ? (unsigned)S.row_index(u1, h * HALF + RA[i]) * (unsigned)(K * 2) + CA2[i] : gc[h][i]; } }
.LBB0_1688:
	v_add_u32_e32 v6, 0x80, v164
	v_add_u32_e32 v8, s7, v6
	v_cmp_gt_i32_e32 vcc, s8, v8
	v_mov_b32_e32 v154, 0
	s_and_saveexec_b64 s[0:1], vcc
	s_cbranch_execz .LBB0_1690
	v_add_u32_e32 v8, s15, v8
	v_readlane_b32 s4, v251, 3
	v_ashrrev_i32_e32 v9, 31, v8
	v_readlane_b32 s5, v251, 4
	s_nop 1
	v_lshl_add_u64 v[8:9], v[8:9], 2, s[4:5]
	global_load_dword v154, v[8:9], off
.LBB0_1690:
	s_or_b64 exec, exec, s[0:1]
	s_and_b64 vcc, exec, s[42:43]
	s_cbranch_vccnz .LBB0_1694
	v_add_u32_e32 v7, s13, v6
	v_cmp_gt_i32_e32 vcc, s14, v7
	v_mov_b32_e32 v168, 0
	s_and_saveexec_b64 s[0:1], vcc
	s_cbranch_execz .LBB0_1693
	v_add_u32_e32 v6, s12, v7
	v_readlane_b32 s4, v251, 3
	v_ashrrev_i32_e32 v7, 31, v6
	v_readlane_b32 s5, v251, 4
	s_nop 1
	v_lshl_add_u64 v[6:7], v[6:7], 2, s[4:5]
	global_load_dword v168, v[6:7], off

; #define PG8_STAGE(bufoff, gbase, voff) do { _Pragma("unroll") for (int _i = 0; _i < 2; ++_i) \
;         __builtin_amdgcn_global_load_lds((const unsigned*)((const char*)(gbase) + (voff)[_i]), (PG8_LAS unsigned*)(lds + (bufoff) + ldsw + _i * 8192), 16, 0, 0); } while (0)
; #define PG8_STAGE_G(bufoff, kb, g) do { _Pragma("unroll") for (int _i = 0; _i < 2; ++_i) \
;         __builtin_amdgcn_global_load_lds((const unsigned*)(gA + (size_t)(kb) + (g)[_i]), (PG8_LAS unsigned*)(lds + (bufoff) + ldsw + _i * 8192), 16, 0, 0); } while (0)
; #define PG8_WAIT_V(n) asm volatile("s_waitcnt vmcnt(" #n ")" ::: "memory")
; #define PG8_BAR __builtin_amdgcn_s_barrier()
; template <class Epi, class Sched, bool ALIGN_EPI = false, bool SP2 = false, bool GATHER = false, bool HALFM = false>
; __device__ __forceinline__ void gemm_phase(PG8_LAS unsigned char* lds, const int Kdim, const Sched& S, const Epi& E) {
;     ...
;             for (int i = 0; i < 2; ++i) { gc[h][i] = (unsigned)S.row_index(cur, h * HALF + RA[i]) * (unsigned)(K * 2) + CA2[i]; gn[h][i] = h1 ? (unsigned)S.row_index(u1, h * HALF + RA[i]) * (unsigned)(K * 2) + CA2[i] : gc[h][i]; } }
;     if constexpr (SP2) {
;         PG8_STAGE(PG8_SB(0, 0), cB, voffB); PG8_STAGE(PG8_SB(0, 1), cB + hstep, voffB);
;         if constexpr (GATHER) { PG8_STAGE_G(PG8_SA(0, 0), 0, gc[0]); PG8_STAGE_G(PG8_SA(0, 1), 0, gc[1]); } else { PG8_STAGE(PG8_SA(0, 0), cA, voffA); PG8_STAGE(PG8_SA(0, 1), cA + hstep, voffA); }
;         if (wr == 1) PG8_BAR;
;         PG8_WAIT_V(2); PG8_BAR;
;         PG8_STAGE(PG8_SB(1, 0), cB + kstep, voffB); if constexpr (GATHER) PG8_STAGE_G(PG8_SA(1, 0), kstep, gc[0]); else PG8_STAGE(PG8_SA(1, 0), cA + kstep, voffA); PG8_STAGE(PG8_SB(1, 1), cB + hstep + kstep, voffB);
.LBB0_1694:
	s_waitcnt vmcnt(0)
	v_lshl_add_u32 v148, v148, 11, v162
	v_lshl_add_u32 v150, v150, 11, v165
	v_lshl_add_u32 v152, v152, 11, v162
	v_lshl_add_u32 v154, v154, 11, v165
	v_lshl_add_u32 v163, v163, 11, v162
	v_lshl_add_u32 v166, v166, 11, v165
	v_lshl_add_u32 v167, v167, 11, v162
	v_lshl_add_u32 v168, v168, 11, v165
	v_cndmask_b32_e64 v163, v163, v148, s[42:43]
	v_cndmask_b32_e64 v166, v166, v150, s[42:43]
	v_cndmask_b32_e64 v167, v167, v152, s[42:43]
	v_cndmask_b32_e64 v168, v168, v154, s[42:43]
	v_lshlrev_b32_e32 v6, 1, v1
	v_lshrrev_b32_e32 v7, 2, v1
	v_and_b32_e32 v4, 3, v4
	s_mov_b32 s0, 0x1fffe0
	s_ashr_i32 s4, s6, 6
	v_and_b32_e32 v6, 24, v6
	v_and_b32_e32 v7, 4, v7
	v_and_or_b32 v4, v1, s0, v4
	v_or3_b32 v4, v4, v7, v6
	s_lshl_b32 s8, s4, 10
	v_lshl_add_u32 v156, v4, 11, v162
	v_lshlrev_b32_e32 v4, 1, v164
	v_lshrrev_b32_e32 v6, 2, v164
	v_and_b32_e32 v5, 3, v5
	s_add_i32 s12, s8, 0
	v_and_b32_e32 v4, 24, v4
	v_and_b32_e32 v6, 4, v6
	v_and_or_b32 v5, v164, s0, v5
	s_add_i32 m0, s12, 0x10000
	v_or3_b32 v4, v5, v6, v4
	s_ashr_i32 s5, s6, 8
	global_load_lds_dwordx4 v156, s[40:41]
	s_add_i32 m0, s12, 0x12000
	v_lshl_add_u32 v158, v4, 11, v165
	s_add_u32 s0, s40, 0x40000
	global_load_lds_dwordx4 v158, s[40:41]
	s_addc_u32 s1, s41, 0
	s_add_i32 m0, s12, 0x14000
	s_add_i32 s13, s12, 0x2000
	global_load_lds_dwordx4 v156, s[0:1]
	s_add_i32 m0, s12, 0x16000
	s_add_i32 s22, s12, 0x4000
	global_load_lds_dwordx4 v158, s[0:1]
	s_mov_b32 m0, s12
	s_add_i32 s23, s12, 0x6000
	global_load_lds_dwordx4 v148, s[78:79]
	s_mov_b32 m0, s13
	v_mov_b32_e32 v157, v3
	global_load_lds_dwordx4 v150, s[78:79]
	s_mov_b32 m0, s22
	v_mov_b32_e32 v159, v3
	global_load_lds_dwordx4 v152, s[78:79]
	s_mov_b32 m0, s23
	s_cmp_eq_u32 s5, 1
	global_load_lds_dwordx4 v154, s[78:79]
	v_lshl_add_u64 v[4:5], s[40:41], 0, v[156:157]
	s_cselect_b64 s[0:1], -1, 0
	s_cmp_lg_u32 s5, 1
	v_lshl_add_u64 v[6:7], s[40:41], 0, v[158:159]
	s_cbranch_scc1 .LBB0_1696
	s_barrier

; #define PG8_STAGE(bufoff, gbase, voff) do { _Pragma("unroll") for (int _i = 0; _i < 2; ++_i) \
;         __builtin_amdgcn_global_load_lds((const unsigned*)((const char*)(gbase) + (voff)[_i]), (PG8_LAS unsigned*)(lds + (bufoff) + ldsw + _i * 8192), 16, 0, 0); } while (0)
; #define PG8_WAIT_V(n) asm volatile("s_waitcnt vmcnt(" #n ")" ::: "memory")
; #define PG8_WAIT_L(n) asm volatile("s_waitcnt lgkmcnt(" #n ")" ::: "memory")
; template <class Epi, class Sched, bool ALIGN_EPI = false, bool SP2 = false, bool GATHER = false, bool HALFM = false>
; __device__ __forceinline__ void gemm_phase(PG8_LAS unsigned char* lds, const int Kdim, const Sched& S, const Epi& E) {
;     ...
;         for (int t = 0; t < nt; t += 2) {
;             const bool last = (t == nt - 2);
;             const char* a1 = cA + (size_t)(t + 1) * kstep;
;             const char* a2 = last ? nA : cA + (size_t)(t + 2) * kstep; const char* b2 = last ? nB : cB + (size_t)(t + 2) * kstep;
;             const char* a3 = a2 + kstep; const char* b3 = b2 + kstep;
;             if (last && has_next) S.a_ready(nxt);
;             unsigned s0[2] = {0u, 0u}, s1[2] = {0u, 0u}; size_t kb2 = 0;
;             if constexpr (GATHER) { kb2 = last ? (size_t)0 : (size_t)(t + 2) * kstep;
; #pragma unroll
;                 for (int i = 0; i < 2; ++i) { s0[i] = last ? gn[0][i] : gc[0][i]; s1[i] = last ? gn[1][i] : gc[1][i]; } }
;             if constexpr (SP2) {
;             PG8_LDB(B0, 0, 0); PG8_LDB(B1, 0, 1); PG8_SCHED; PG8_LDA(At, 0, 0); if constexpr (GATHER) PG8_STAGE_G(PG8_SA(1, 1), (size_t)(t + 1) * kstep, gc[1]); else PG8_STAGE(PG8_SA(1, 1), a1 + hstep, voffA);
;             PG8_WAIT_V(8); PG8_WAIT_L(0); PG8_BAR; PG8_MMA(0, 0, At, B0); PG8_MMA(0, 1, At, B1); PG8_BAR; PG8_SCHED;
;             if constexpr (!HALFM) PG8_LDA(At, 0, 1); PG8_STAGE(PG8_SB(0, 0), b2, voffB); PG8_STAGE(PG8_SB(0, 1), b2 + hstep, voffB); if constexpr (GATHER) PG8_STAGE_G(PG8_SA(0, 0), kb2, s0); else PG8_STAGE(PG8_SA(0, 0), a2, voffA);
;             PG8_WAIT_V(8); PG8_WAIT_L(0); PG8_BAR; if constexpr (!HALFM) { PG8_MMA(1, 0, At, B0); PG8_MMA(1, 1, At, B1); } PG8_BAR; PG8_SCHED;
;             PG8_LDB(B0, 1, 0); PG8_LDB(B1, 1, 1); PG8_SCHED; PG8_LDA(At, 1, 0); if constexpr (GATHER) PG8_STAGE_G(PG8_SA(0, 1), kb2, s1); else PG8_STAGE(PG8_SA(0, 1), a2 + hstep, voffA);
;     ...
;         if constexpr (ALIGN_EPI) { if (wr == 1) PG8_BAR; }
.LBB0_1715:
	s_add_u32 s36, s40, 0x100
	s_addc_u32 s82, s41, 0
	s_and_b64 s[4:5], s[44:45], exec
	v_readlane_b32 s4, v251, 8
	v_mov_b32_e32 v153, v3
	v_mov_b32_e32 v155, v3
	v_readlane_b32 s5, v251, 9
	s_cselect_b32 s41, s17, s41
	s_cselect_b32 s40, s16, s40
	v_lshl_add_u64 v[132:133], s[4:5], 0, v[154:155]
	v_lshl_add_u64 v[134:135], s[4:5], 0, v[152:153]
	s_mov_b32 s83, -2
	s_mov_b64 s[14:15], 0
	s_cmp_eq_u32 s76, 0
	s_cbranch_scc1 .Lup_unit_nobar
	s_cmp_eq_u64 s[0:1], 0
	s_cbranch_scc1 .Lup_unit_nobar
	s_barrier
.Lup_unit_nobar:
.LBB0_1716:
	s_add_u32 s20, s36, s14
	s_addc_u32 s21, s82, s15
	s_add_u32 s24, s14, 0x100
	s_addc_u32 s25, s15, 0
	s_cmpk_eq_i32 s14, 0x700
	s_cselect_b64 vcc, -1, 0
	s_and_b64 s[4:5], vcc, exec
	s_cselect_b32 s5, s41, s21
	s_cselect_b32 s4, s40, s20
	s_cselect_b32 s20, 0, s24
	s_add_i32 s21, 0, 0x10000
	v_add_u32_e32 v161, s21, v170
	s_add_i32 s33, 0, 0x14000
	ds_read_b128 v[136:139], v161
	ds_read_b128 v[140:143], v161 offset:1024
	ds_read_b128 v[144:147], v161 offset:2048
	ds_read_b128 v[182:185], v161 offset:3072
	v_add_u32_e32 v161, s33, v170
	ds_read_b128 v[186:189], v161
	ds_read_b128 v[190:193], v161 offset:1024
	ds_read_b128 v[194:197], v161 offset:2048
	ds_read_b128 v[198:201], v161 offset:3072
	v_cndmask_b32_e32 v2, v148, v163, vcc
	v_cndmask_b32_e32 v153, v152, v167, vcc
	v_cndmask_b32_e32 v160, v150, v166, vcc
	v_cndmask_b32_e32 v155, v154, v168, vcc
	v_lshl_add_u64 v[220:221], v[134:135], 0, s[14:15]
	s_add_i32 m0, s12, 0xc000
	ds_read_b128 v[202:205], v177
	ds_read_b128 v[208:211], v177 offset:1024
	ds_read_b128 v[224:227], v177 offset:2048
	ds_read_b128 v[228:231], v177 offset:3072
	ds_read_b128 v[232:235], v177 offset:4096
	ds_read_b128 v[236:239], v177 offset:5120
	ds_read_b128 v[240:243], v177 offset:6144
	ds_read_b128 v[244:247], v177 offset:7168
	global_load_lds_dwordx4 v[220:221], off
	v_lshl_add_u64 v[220:221], v[132:133], 0, s[14:15]
	s_add_i32 m0, s12, 0xe000
	s_nop 0
	global_load_lds_dwordx4 v[220:221], off
	s_waitcnt vmcnt(8)
	s_waitcnt lgkmcnt(0)
	s_barrier
	s_setprio 1
	s_waitcnt lgkmcnt(0)
	v_mfma_f32_16x16x32_bf16 v[128:131], v[136:139], v[202:205], v[128:131]
	v_mfma_f32_16x16x32_bf16 v[124:127], v[144:147], v[202:205], v[124:127]
	v_mfma_f32_16x16x32_bf16 v[120:123], v[136:139], v[224:227], v[120:123]
	v_mfma_f32_16x16x32_bf16 v[116:119], v[144:147], v[224:227], v[116:119]
	v_mfma_f32_16x16x32_bf16 v[112:115], v[136:139], v[232:235], v[112:115]
	v_mfma_f32_16x16x32_bf16 v[108:111], v[144:147], v[232:235], v[108:111]
	v_mfma_f32_16x16x32_bf16 v[104:107], v[136:139], v[240:243], v[104:107]
	v_mfma_f32_16x16x32_bf16 v[100:103], v[144:147], v[240:243], v[100:103]
	v_mfma_f32_16x16x32_bf16 v[128:131], v[140:143], v[208:211], v[128:131]
	v_mfma_f32_16x16x32_bf16 v[124:127], v[182:185], v[208:211], v[124:127]
	v_mfma_f32_16x16x32_bf16 v[120:123], v[140:143], v[228:231], v[120:123]
	v_mfma_f32_16x16x32_bf16 v[116:119], v[182:185], v[228:231], v[116:119]
	v_mfma_f32_16x16x32_bf16 v[112:115], v[140:143], v[236:239], v[112:115]
	v_mfma_f32_16x16x32_bf16 v[108:111], v[182:185], v[236:239], v[108:111]
	v_mfma_f32_16x16x32_bf16 v[104:107], v[140:143], v[244:247], v[104:107]
	v_mfma_f32_16x16x32_bf16 v[100:103], v[182:185], v[244:247], v[100:103]
	s_setprio 0
	s_setprio 1
	v_mfma_f32_16x16x32_bf16 v[96:99], v[186:189], v[202:205], v[96:99]
	v_mfma_f32_16x16x32_bf16 v[92:95], v[194:197], v[202:205], v[92:95]
	v_mfma_f32_16x16x32_bf16 v[88:91], v[186:189], v[224:227], v[88:91]
	v_mfma_f32_16x16x32_bf16 v[84:87], v[194:197], v[224:227], v[84:87]
	v_mfma_f32_16x16x32_bf16 v[80:83], v[186:189], v[232:235], v[80:83]
	v_mfma_f32_16x16x32_bf16 v[76:79], v[194:197], v[232:235], v[76:79]
	v_mfma_f32_16x16x32_bf16 v[72:75], v[186:189], v[240:243], v[72:75]
	v_mfma_f32_16x16x32_bf16 v[68:71], v[194:197], v[240:243], v[68:71]
	v_mfma_f32_16x16x32_bf16 v[96:99], v[190:193], v[208:211], v[96:99]
	v_mfma_f32_16x16x32_bf16 v[92:95], v[198:201], v[208:211], v[92:95]
	v_mfma_f32_16x16x32_bf16 v[88:91], v[190:193], v[228:231], v[88:91]
	v_mfma_f32_16x16x32_bf16 v[84:87], v[198:201], v[228:231], v[84:87]
	v_mfma_f32_16x16x32_bf16 v[80:83], v[190:193], v[236:239], v[80:83]
	v_mfma_f32_16x16x32_bf16 v[76:79], v[198:201], v[236:239], v[76:79]
	v_mfma_f32_16x16x32_bf16 v[72:75], v[190:193], v[244:247], v[72:75]
	v_mfma_f32_16x16x32_bf16 v[68:71], v[198:201], v[244:247], v[68:71]
	s_setprio 0
	s_barrier
	s_add_i32 s14, s21, s8
	v_lshl_add_u64 v[220:221], s[4:5], 0, v[156:157]
	s_mov_b32 m0, s14
	ds_read_b128 v[202:205], v177 offset:16384
	ds_read_b128 v[208:211], v177 offset:17408
	ds_read_b128 v[224:227], v177 offset:18432
	ds_read_b128 v[228:231], v177 offset:19456
	ds_read_b128 v[232:235], v177 offset:20480
	ds_read_b128 v[236:239], v177 offset:21504
	ds_read_b128 v[240:243], v177 offset:22528
	ds_read_b128 v[244:247], v177 offset:23552
	global_load_lds_dwordx4 v[220:221], off
	s_add_i32 m0, s14, 0x2000
	s_add_u32 s14, s4, 0x40000
	v_lshl_add_u64 v[216:217], s[4:5], 0, v[158:159]
	s_addc_u32 s15, s5, 0
	s_add_i32 s21, s33, s8
	global_load_lds_dwordx4 v[216:217], off
	v_lshl_add_u64 v[218:219], s[14:15], 0, v[156:157]
	s_mov_b32 m0, s21
	v_mov_b32_e32 v161, v3
	global_load_lds_dwordx4 v[218:219], off
	s_add_i32 m0, s21, 0x2000
	v_lshl_add_u64 v[218:219], s[14:15], 0, v[158:159]
	s_add_u32 s14, s78, s20
	global_load_lds_dwordx4 v[218:219], off
	s_addc_u32 s15, s79, 0
	s_mov_b32 m0, s12
	v_lshl_add_u64 v[218:219], s[14:15], 0, v[2:3]
	global_load_lds_dwordx4 v2, s[14:15]
	s_mov_b32 m0, s13
	s_nop 0
	global_load_lds_dwordx4 v160, s[14:15]
	s_waitcnt vmcnt(8)
	s_waitcnt lgkmcnt(0)
	v_lshl_add_u64 v[160:161], s[14:15], 0, v[160:161]
	s_barrier
; #define PG8_STAGE(bufoff, gbase, voff) do { _Pragma("unroll") for (int _i = 0; _i < 2; ++_i) \
;         __builtin_amdgcn_global_load_lds((const unsigned*)((const char*)(gbase) + (voff)[_i]), (PG8_LAS unsigned*)(lds + (bufoff) + ldsw + _i * 8192), 16, 0, 0); } while (0)
; #define PG8_STAGE_G(bufoff, kb, g) do { _Pragma("unroll") for (int _i = 0; _i < 2; ++_i) \
;         __builtin_amdgcn_global_load_lds((const unsigned*)(gA + (size_t)(kb) + (g)[_i]), (PG8_LAS unsigned*)(lds + (bufoff) + ldsw + _i * 8192), 16, 0, 0); } while (0)
; #define PG8_LDA(dst, b, h) do { _Pragma("unroll") for (int m = 0; m < 4; ++m) _Pragma("unroll") for (int k = 0; k < 2; ++k) dst[m][k] = *(const PG8_LAS bf16x8*)(lds + PG8_SA(b, h) + aoff + m * 2048 + k * 1024); } while (0)
; #define PG8_LDB(dst, b, h) do { _Pragma("unroll") for (int n = 0; n < 2; ++n) _Pragma("unroll") for (int k = 0; k < 2; ++k) dst[n][k] = *(const PG8_LAS bf16x8*)(lds + PG8_SB(b, h) + boff + n * 2048 + k * 1024); } while (0)
; #define PG8_MMA(ai, bj, At, Bt) do { __builtin_amdgcn_s_setprio(1); _Pragma("unroll") for (int m = 0; m < 4; ++m) _Pragma("unroll") for (int n = 0; n < 2; ++n) _Pragma("unroll") for (int k = 0; k < 2; ++k) \
;         acc[ai][bj][m][n] = __builtin_amdgcn_mfma_f32_16x16x32_bf16(Bt[n][k], At[m][k], acc[ai][bj][m][n], 0, 0, 0); __builtin_amdgcn_s_setprio(0); } while (0)
; #define PG8_WAIT_V(n) asm volatile("s_waitcnt vmcnt(" #n ")" ::: "memory")
; #define PG8_WAIT_L(n) asm volatile("s_waitcnt lgkmcnt(" #n ")" ::: "memory")
; #define PG8_BAR __builtin_amdgcn_s_barrier()
; #define PG8_SCHED __builtin_amdgcn_sched_barrier(0)
; template <class Epi, class Sched, bool ALIGN_EPI = false, bool SP2 = false, bool GATHER = false, bool HALFM = false>
; __device__ __forceinline__ void gemm_phase(PG8_LAS unsigned char* lds, const int Kdim, const Sched& S, const Epi& E) {
;     ...
;             PG8_WAIT_V(8); PG8_WAIT_L(0); PG8_BAR; if constexpr (!HALFM) { PG8_MMA(1, 0, At, B0); PG8_MMA(1, 1, At, B1); } PG8_BAR; PG8_SCHED;
;             PG8_LDB(B0, 1, 0); PG8_LDB(B1, 1, 1); PG8_SCHED; PG8_LDA(At, 1, 0); if constexpr (GATHER) PG8_STAGE_G(PG8_SA(0, 1), kb2, s1); else PG8_STAGE(PG8_SA(0, 1), a2 + hstep, voffA);
;             PG8_WAIT_V(8); PG8_WAIT_L(0); PG8_BAR; PG8_MMA(0, 0, At, B0); PG8_MMA(0, 1, At, B1); PG8_BAR; PG8_SCHED;
	s_setprio 1
	s_waitcnt lgkmcnt(0)
	v_mfma_f32_16x16x32_bf16 v[64:67], v[136:139], v[202:205], v[64:67]
	v_mfma_f32_16x16x32_bf16 v[60:63], v[144:147], v[202:205], v[60:63]
	v_mfma_f32_16x16x32_bf16 v[56:59], v[136:139], v[224:227], v[56:59]
	v_mfma_f32_16x16x32_bf16 v[52:55], v[144:147], v[224:227], v[52:55]
	v_mfma_f32_16x16x32_bf16 v[48:51], v[136:139], v[232:235], v[48:51]
	v_mfma_f32_16x16x32_bf16 v[44:47], v[144:147], v[232:235], v[44:47]
	v_mfma_f32_16x16x32_bf16 v[40:43], v[136:139], v[240:243], v[40:43]
	v_mfma_f32_16x16x32_bf16 v[36:39], v[144:147], v[240:243], v[36:39]
	v_mfma_f32_16x16x32_bf16 v[64:67], v[140:143], v[208:211], v[64:67]
	v_mfma_f32_16x16x32_bf16 v[60:63], v[182:185], v[208:211], v[60:63]
	v_mfma_f32_16x16x32_bf16 v[56:59], v[140:143], v[228:231], v[56:59]
	v_mfma_f32_16x16x32_bf16 v[52:55], v[182:185], v[228:231], v[52:55]
	v_mfma_f32_16x16x32_bf16 v[48:51], v[140:143], v[236:239], v[48:51]
	v_mfma_f32_16x16x32_bf16 v[44:47], v[182:185], v[236:239], v[44:47]
	v_mfma_f32_16x16x32_bf16 v[40:43], v[140:143], v[244:247], v[40:43]
	v_mfma_f32_16x16x32_bf16 v[36:39], v[182:185], v[244:247], v[36:39]
	s_setprio 0
	s_setprio 1
	v_mfma_f32_16x16x32_bf16 v[32:35], v[186:189], v[202:205], v[32:35]
	v_mfma_f32_16x16x32_bf16 v[28:31], v[194:197], v[202:205], v[28:31]
	v_mfma_f32_16x16x32_bf16 v[24:27], v[186:189], v[224:227], v[24:27]
	v_mfma_f32_16x16x32_bf16 v[20:23], v[194:197], v[224:227], v[20:23]
	v_mfma_f32_16x16x32_bf16 v[16:19], v[186:189], v[232:235], v[16:19]
	v_mfma_f32_16x16x32_bf16 v[12:15], v[194:197], v[232:235], v[12:15]
	v_mfma_f32_16x16x32_bf16 v[8:11], v[186:189], v[240:243], v[8:11]
	v_mfma_f32_16x16x32_bf16 v[4:7], v[194:197], v[240:243], v[4:7]
	v_mfma_f32_16x16x32_bf16 v[32:35], v[190:193], v[208:211], v[32:35]
	v_mfma_f32_16x16x32_bf16 v[28:31], v[198:201], v[208:211], v[28:31]
	v_mfma_f32_16x16x32_bf16 v[24:27], v[190:193], v[228:231], v[24:27]
	v_mfma_f32_16x16x32_bf16 v[20:23], v[198:201], v[228:231], v[20:23]
	v_mfma_f32_16x16x32_bf16 v[16:19], v[190:193], v[236:239], v[16:19]
	v_mfma_f32_16x16x32_bf16 v[12:15], v[198:201], v[236:239], v[12:15]
	v_mfma_f32_16x16x32_bf16 v[8:11], v[190:193], v[244:247], v[8:11]
	v_mfma_f32_16x16x32_bf16 v[4:7], v[198:201], v[244:247], v[4:7]
	s_setprio 0
	s_barrier
	s_add_i32 s20, 0, 0x18000
	v_add_u32_e32 v2, s20, v170
	s_add_i32 s21, 0, 0x1c000
	ds_read_b128 v[136:139], v2
	ds_read_b128 v[140:143], v2 offset:1024
	ds_read_b128 v[144:147], v2 offset:2048
	ds_read_b128 v[182:185], v2 offset:3072
	v_add_u32_e32 v2, s21, v170
	ds_read_b128 v[186:189], v2
	ds_read_b128 v[190:193], v2 offset:1024
	ds_read_b128 v[194:197], v2 offset:2048
	ds_read_b128 v[198:201], v2 offset:3072
	s_mov_b32 m0, s22
	ds_read_b128 v[202:205], v177 offset:32768
	ds_read_b128 v[208:211], v177 offset:33792
	ds_read_b128 v[224:227], v177 offset:34816
	ds_read_b128 v[228:231], v177 offset:35840
	ds_read_b128 v[232:235], v177 offset:36864
	ds_read_b128 v[236:239], v177 offset:37888
	ds_read_b128 v[240:243], v177 offset:38912
	ds_read_b128 v[244:247], v177 offset:39936
	global_load_lds_dwordx4 v153, s[14:15]
	s_mov_b32 m0, s23
	s_nop 0
	global_load_lds_dwordx4 v155, s[14:15]
	s_waitcnt vmcnt(8)
	s_waitcnt lgkmcnt(0)
	s_barrier
	s_setprio 1
	s_waitcnt lgkmcnt(0)
	v_mfma_f32_16x16x32_bf16 v[128:131], v[136:139], v[202:205], v[128:131]
	v_mfma_f32_16x16x32_bf16 v[124:127], v[144:147], v[202:205], v[124:127]
	v_mfma_f32_16x16x32_bf16 v[120:123], v[136:139], v[224:227], v[120:123]
	v_mfma_f32_16x16x32_bf16 v[116:119], v[144:147], v[224:227], v[116:119]
	v_mfma_f32_16x16x32_bf16 v[112:115], v[136:139], v[232:235], v[112:115]
	v_mfma_f32_16x16x32_bf16 v[108:111], v[144:147], v[232:235], v[108:111]
	v_mfma_f32_16x16x32_bf16 v[104:107], v[136:139], v[240:243], v[104:107]
	v_mfma_f32_16x16x32_bf16 v[100:103], v[144:147], v[240:243], v[100:103]
	v_mfma_f32_16x16x32_bf16 v[128:131], v[140:143], v[208:211], v[128:131]
	v_mfma_f32_16x16x32_bf16 v[124:127], v[182:185], v[208:211], v[124:127]
	v_mfma_f32_16x16x32_bf16 v[120:123], v[140:143], v[228:231], v[120:123]
	v_mfma_f32_16x16x32_bf16 v[116:119], v[182:185], v[228:231], v[116:119]
	v_mfma_f32_16x16x32_bf16 v[112:115], v[140:143], v[236:239], v[112:115]
	v_mfma_f32_16x16x32_bf16 v[108:111], v[182:185], v[236:239], v[108:111]
	v_mfma_f32_16x16x32_bf16 v[104:107], v[140:143], v[244:247], v[104:107]
	v_mfma_f32_16x16x32_bf16 v[100:103], v[182:185], v[244:247], v[100:103]
	s_setprio 0
	s_setprio 1
	v_mfma_f32_16x16x32_bf16 v[96:99], v[186:189], v[202:205], v[96:99]
	v_mfma_f32_16x16x32_bf16 v[92:95], v[194:197], v[202:205], v[92:95]
	v_mfma_f32_16x16x32_bf16 v[88:91], v[186:189], v[224:227], v[88:91]
	v_mfma_f32_16x16x32_bf16 v[84:87], v[194:197], v[224:227], v[84:87]
	v_mfma_f32_16x16x32_bf16 v[80:83], v[186:189], v[232:235], v[80:83]
	v_mfma_f32_16x16x32_bf16 v[76:79], v[194:197], v[232:235], v[76:79]
	v_mfma_f32_16x16x32_bf16 v[72:75], v[186:189], v[240:243], v[72:75]
	v_mfma_f32_16x16x32_bf16 v[68:71], v[194:197], v[240:243], v[68:71]
	v_mfma_f32_16x16x32_bf16 v[96:99], v[190:193], v[208:211], v[96:99]
	v_mfma_f32_16x16x32_bf16 v[92:95], v[198:201], v[208:211], v[92:95]
	v_mfma_f32_16x16x32_bf16 v[88:91], v[190:193], v[228:231], v[88:91]
	v_mfma_f32_16x16x32_bf16 v[84:87], v[198:201], v[228:231], v[84:87]
	v_mfma_f32_16x16x32_bf16 v[80:83], v[190:193], v[236:239], v[80:83]
	v_mfma_f32_16x16x32_bf16 v[76:79], v[198:201], v[236:239], v[76:79]
	v_mfma_f32_16x16x32_bf16 v[72:75], v[190:193], v[244:247], v[72:75]
	v_mfma_f32_16x16x32_bf16 v[68:71], v[198:201], v[244:247], v[68:71]
	s_setprio 0
	s_barrier
; #define PG8_STAGE(bufoff, gbase, voff) do { _Pragma("unroll") for (int _i = 0; _i < 2; ++_i) \
;         __builtin_amdgcn_global_load_lds((const unsigned*)((const char*)(gbase) + (voff)[_i]), (PG8_LAS unsigned*)(lds + (bufoff) + ldsw + _i * 8192), 16, 0, 0); } while (0)
; #define PG8_STAGE_G(bufoff, kb, g) do { _Pragma("unroll") for (int _i = 0; _i < 2; ++_i) \
;         __builtin_amdgcn_global_load_lds((const unsigned*)(gA + (size_t)(kb) + (g)[_i]), (PG8_LAS unsigned*)(lds + (bufoff) + ldsw + _i * 8192), 16, 0, 0); } while (0)
; #define PG8_LDA(dst, b, h) do { _Pragma("unroll") for (int m = 0; m < 4; ++m) _Pragma("unroll") for (int k = 0; k < 2; ++k) dst[m][k] = *(const PG8_LAS bf16x8*)(lds + PG8_SA(b, h) + aoff + m * 2048 + k * 1024); } while (0)
; #define PG8_MMA(ai, bj, At, Bt) do { __builtin_amdgcn_s_setprio(1); _Pragma("unroll") for (int m = 0; m < 4; ++m) _Pragma("unroll") for (int n = 0; n < 2; ++n) _Pragma("unroll") for (int k = 0; k < 2; ++k) \
;         acc[ai][bj][m][n] = __builtin_amdgcn_mfma_f32_16x16x32_bf16(Bt[n][k], At[m][k], acc[ai][bj][m][n], 0, 0, 0); __builtin_amdgcn_s_setprio(0); } while (0)
; #define PG8_WAIT_V(n) asm volatile("s_waitcnt vmcnt(" #n ")" ::: "memory")
; #define PG8_WAIT_L(n) asm volatile("s_waitcnt lgkmcnt(" #n ")" ::: "memory")
; #define PG8_BAR __builtin_amdgcn_s_barrier()
; template <class Epi, class Sched, bool ALIGN_EPI = false, bool SP2 = false, bool GATHER = false, bool HALFM = false>
; __device__ __forceinline__ void gemm_phase(PG8_LAS unsigned char* lds, const int Kdim, const Sched& S, const Epi& E) {
;     ...
;             if constexpr (!HALFM) PG8_LDA(At, 1, 1); PG8_STAGE(PG8_SB(1, 0), b3, voffB); PG8_STAGE(PG8_SB(1, 1), b3 + hstep, voffB); if constexpr (GATHER) PG8_STAGE_G(PG8_SA(1, 0), kb2 + kstep, s0); else PG8_STAGE(PG8_SA(1, 0), a3, voffA);
;             PG8_WAIT_V(8); PG8_WAIT_L(0); PG8_BAR; if constexpr (!HALFM) { PG8_MMA(1, 0, At, B0); PG8_MMA(1, 1, At, B1); } PG8_BAR; PG8_SCHED;
;     __device__ __forceinline__ void operator()(const pg8::f32x4 (&acc)[2][2][4][2], const pg8::Unit& u, int wr, int wc, int fr, int fq) const {
;     ...
;         const int colj = u.pn * 128 + wc * 32 + 8 * fq;
;         const float* bg = b_up + u.e * 2048 + colj;
;         f32x4 bgv[2], blv[2];
; #pragma unroll
;         for (int n = 0; n < 2; ++n) { bgv[n] = *(const f32x4*)(bg + 4 * n); blv[n] = *(const f32x4*)(bg + 1024 + 4 * n); }
	s_add_i32 s14, s20, s8
	v_lshl_add_u64 v[220:221], v[220:221], 0, s[34:35]
	s_mov_b32 m0, s14
	ds_read_b128 v[202:205], v177 offset:49152
	ds_read_b128 v[208:211], v177 offset:50176
	ds_read_b128 v[224:227], v177 offset:51200
	ds_read_b128 v[228:231], v177 offset:52224
	ds_read_b128 v[232:235], v177 offset:53248
	ds_read_b128 v[236:239], v177 offset:54272
	ds_read_b128 v[240:243], v177 offset:55296
	ds_read_b128 v[244:247], v177 offset:56320
	global_load_lds_dwordx4 v[220:221], off
	s_add_i32 m0, s14, 0x2000
	s_add_u32 s4, s4, 0x40080
	v_lshl_add_u64 v[216:217], v[216:217], 0, s[34:35]
	s_addc_u32 s5, s5, 0
	s_add_i32 s14, s21, s8
	global_load_lds_dwordx4 v[216:217], off
	v_lshl_add_u64 v[216:217], s[4:5], 0, v[156:157]
	s_mov_b32 m0, s14
	v_lshl_add_u64 v[160:161], v[160:161], 0, s[34:35]
	global_load_lds_dwordx4 v[216:217], off
	v_lshl_add_u64 v[216:217], s[4:5], 0, v[158:159]
	s_add_i32 m0, s14, 0x2000
	s_nop 0
	global_load_lds_dwordx4 v[216:217], off
	v_lshl_add_u64 v[216:217], v[218:219], 0, s[34:35]
	s_mov_b32 m0, s50
	s_nop 0
	global_load_lds_dwordx4 v[216:217], off
	s_mov_b32 m0, s51
	s_nop 0
	global_load_lds_dwordx4 v[160:161], off
	s_waitcnt vmcnt(8)
	s_waitcnt lgkmcnt(0)
	s_barrier
	s_setprio 1
	s_waitcnt lgkmcnt(0)
	v_mfma_f32_16x16x32_bf16 v[64:67], v[136:139], v[202:205], v[64:67]
	v_mfma_f32_16x16x32_bf16 v[60:63], v[144:147], v[202:205], v[60:63]
	v_mfma_f32_16x16x32_bf16 v[56:59], v[136:139], v[224:227], v[56:59]
	v_mfma_f32_16x16x32_bf16 v[52:55], v[144:147], v[224:227], v[52:55]
	v_mfma_f32_16x16x32_bf16 v[48:51], v[136:139], v[232:235], v[48:51]
	v_mfma_f32_16x16x32_bf16 v[44:47], v[144:147], v[232:235], v[44:47]
	v_mfma_f32_16x16x32_bf16 v[40:43], v[136:139], v[240:243], v[40:43]
	v_mfma_f32_16x16x32_bf16 v[36:39], v[144:147], v[240:243], v[36:39]
	v_mfma_f32_16x16x32_bf16 v[64:67], v[140:143], v[208:211], v[64:67]
	v_mfma_f32_16x16x32_bf16 v[60:63], v[182:185], v[208:211], v[60:63]
	v_mfma_f32_16x16x32_bf16 v[56:59], v[140:143], v[228:231], v[56:59]
	v_mfma_f32_16x16x32_bf16 v[52:55], v[182:185], v[228:231], v[52:55]
	v_mfma_f32_16x16x32_bf16 v[48:51], v[140:143], v[236:239], v[48:51]
	v_mfma_f32_16x16x32_bf16 v[44:47], v[182:185], v[236:239], v[44:47]
	v_mfma_f32_16x16x32_bf16 v[40:43], v[140:143], v[244:247], v[40:43]
	v_mfma_f32_16x16x32_bf16 v[36:39], v[182:185], v[244:247], v[36:39]
	s_setprio 0
	s_setprio 1
	v_mfma_f32_16x16x32_bf16 v[32:35], v[186:189], v[202:205], v[32:35]
	v_mfma_f32_16x16x32_bf16 v[28:31], v[194:197], v[202:205], v[28:31]
	v_mfma_f32_16x16x32_bf16 v[24:27], v[186:189], v[224:227], v[24:27]
	v_mfma_f32_16x16x32_bf16 v[20:23], v[194:197], v[224:227], v[20:23]
	v_mfma_f32_16x16x32_bf16 v[16:19], v[186:189], v[232:235], v[16:19]
	v_mfma_f32_16x16x32_bf16 v[12:15], v[194:197], v[232:235], v[12:15]
	v_mfma_f32_16x16x32_bf16 v[8:11], v[186:189], v[240:243], v[8:11]
	v_mfma_f32_16x16x32_bf16 v[4:7], v[194:197], v[240:243], v[4:7]
	v_mfma_f32_16x16x32_bf16 v[32:35], v[190:193], v[208:211], v[32:35]
	v_mfma_f32_16x16x32_bf16 v[28:31], v[198:201], v[208:211], v[28:31]
	v_mfma_f32_16x16x32_bf16 v[24:27], v[190:193], v[228:231], v[24:27]
	v_mfma_f32_16x16x32_bf16 v[20:23], v[198:201], v[228:231], v[20:23]
	v_mfma_f32_16x16x32_bf16 v[16:19], v[190:193], v[236:239], v[16:19]
	v_mfma_f32_16x16x32_bf16 v[12:15], v[198:201], v[236:239], v[12:15]
	v_mfma_f32_16x16x32_bf16 v[8:11], v[190:193], v[244:247], v[8:11]
	v_mfma_f32_16x16x32_bf16 v[4:7], v[198:201], v[244:247], v[4:7]
	s_setprio 0
	s_barrier
	s_add_i32 s83, s83, 2
	s_cmp_gt_u32 s83, 13
	s_mov_b64 s[14:15], s[24:25]
	s_cbranch_scc0 .LBB0_1716
	s_and_b64 vcc, exec, s[6:7]
	s_cbranch_vccz .LBB0_1719
	s_barrier
.LBB0_1719:
	s_add_u32 s40, s36, 0xffffff00
	s_addc_u32 s41, s82, -1
	s_lshl_b32 s4, s46, 11
	s_ashr_i32 s5, s4, 31
	s_lshl_b64 s[4:5], s[4:5], 2
	v_lshl_or_b32 v160, s47, 7, v149
	s_add_u32 s4, s37, s4
	s_addc_u32 s5, s49, s5
	v_ashrrev_i32_e32 v161, 31, v160
	v_lshl_add_u64 v[136:137], v[160:161], 2, s[4:5]
	global_load_dwordx4 v[132:135], v[136:137], off offset:16
	global_load_dwordx4 v[140:143], v[136:137], off
	s_mov_b64 s[4:5], 0x1000
	v_lshl_add_u64 v[138:139], v[136:137], 0, s[4:5]
	v_add_co_u32_e32 v136, vcc, s97, v136
	v_lshlrev_b64 v[160:161], 1, v[160:161]
	s_nop 0
	v_addc_co_u32_e32 v137, vcc, 0, v137, vcc
	global_load_dwordx4 v[144:147], v[136:137], off
	s_nop 0
	global_load_dwordx4 v[136:139], v[138:139], off offset:16
	s_andn2_b64 vcc, exec, s[44:45]
	s_movk_i32 s33, 0x1dff
	s_waitcnt vmcnt(0)
; __device__ __forceinline__ unsigned cvt_pk_bf16(float lo, float hi) { unsigned r; asm volatile("v_cvt_pk_bf16_f32 %0, %1, %2" : "=v"(r) : "v"(lo), "v"(hi)); return r; }
;     __device__ __forceinline__ void operator()(const pg8::f32x4 (&acc)[2][2][4][2], const pg8::Unit& u, int wr, int wc, int fr, int fq) const {
;     ...
;             for (int m = 0; m < 4; ++m) {
;                 const int row = u.pm + ai * 128 + wr * 64 + m * 16 + fr;
;                 float a[8];
; #pragma unroll
;                 for (int n = 0; n < 2; ++n)
; #pragma unroll
;                     for (int j = 0; j < 4; ++j) {
;                         const float g = fminf(acc[ai][0][m][n][j] + bgv[n][j], 7.f);
;                         const float l = fminf(fmaxf(acc[ai][1][m][n][j] + blv[n][j], -7.f), 7.f);
;                         const float sg = __builtin_amdgcn_rcpf(1.f + __builtin_amdgcn_exp2f(-1.702f * 1.4426950408889634f * g));
;                         a[n * 4 + j] = g * sg * (l + 1.f);
;                     }
;                 pg8::u32x4 w; w.x = pg8::cvt_pk_bf16(a[0], a[1]); w.y = pg8::cvt_pk_bf16(a[2], a[3]); w.z = pg8::cvt_pk_bf16(a[4], a[5]); w.w = pg8::cvt_pk_bf16(a[6], a[7]);
	v_add_f32_e32 v2, v128, v140
	v_min_f32_e32 v2, 0x40e00000, v2
	v_mul_f32_e32 v155, 0xc01d265f, v2
	v_exp_f32_e32 v155, v155
	v_add_f32_e32 v153, v96, v144
	v_add_f32_e32 v155, 1.0, v155
	v_rcp_f32_e32 v155, v155
	v_med3_f32 v153, v153, s81, v222
	v_add_f32_e32 v153, 1.0, v153
	v_mul_f32_e32 v2, v2, v155
	v_mul_f32_e32 v2, v153, v2
	v_add_f32_e32 v153, v129, v141
	v_min_f32_e32 v153, 0x40e00000, v153
	v_mul_f32_e32 v182, 0xc01d265f, v153
	v_exp_f32_e32 v182, v182
	v_add_f32_e32 v155, v97, v145
	v_med3_f32 v155, v155, s81, v222
	v_add_f32_e32 v155, 1.0, v155
	v_add_f32_e32 v182, 1.0, v182
	v_rcp_f32_e32 v182, v182
	s_nop 0
	v_mul_f32_e32 v153, v153, v182
	v_mul_f32_e32 v153, v155, v153
	v_add_f32_e32 v155, v130, v142
	v_min_f32_e32 v155, 0x40e00000, v155
	v_mul_f32_e32 v183, 0xc01d265f, v155
	v_exp_f32_e32 v183, v183
	v_add_f32_e32 v182, v98, v146
	v_med3_f32 v182, v182, s81, v222
	v_add_f32_e32 v182, 1.0, v182
	v_add_f32_e32 v183, 1.0, v183
	v_rcp_f32_e32 v183, v183
	s_nop 0
	v_mul_f32_e32 v155, v155, v183
	v_mul_f32_e32 v155, v182, v155
	v_add_f32_e32 v182, v131, v143
	v_min_f32_e32 v182, 0x40e00000, v182
	v_mul_f32_e32 v184, 0xc01d265f, v182
	v_exp_f32_e32 v184, v184
	v_add_f32_e32 v183, v99, v147
	v_med3_f32 v183, v183, s81, v222
	v_add_f32_e32 v183, 1.0, v183
	v_add_f32_e32 v184, 1.0, v184
	v_rcp_f32_e32 v184, v184
	s_nop 0
	v_mul_f32_e32 v182, v182, v184
	v_mul_f32_e32 v182, v183, v182
	v_add_f32_e32 v183, v124, v132
	v_min_f32_e32 v183, 0x40e00000, v183
	v_mul_f32_e32 v185, 0xc01d265f, v183
	v_exp_f32_e32 v185, v185
	v_add_f32_e32 v184, v92, v136
	v_med3_f32 v184, v184, s81, v222
	v_add_f32_e32 v184, 1.0, v184
	v_add_f32_e32 v185, 1.0, v185
	v_rcp_f32_e32 v185, v185
	s_nop 0
	v_mul_f32_e32 v183, v183, v185
	v_mul_f32_e32 v183, v184, v183
	v_add_f32_e32 v184, v125, v133
	v_min_f32_e32 v184, 0x40e00000, v184
	v_mul_f32_e32 v186, 0xc01d265f, v184
	v_exp_f32_e32 v186, v186
	v_add_f32_e32 v185, v93, v137
	v_med3_f32 v185, v185, s81, v222
	v_add_f32_e32 v185, 1.0, v185
	v_add_f32_e32 v186, 1.0, v186
	v_rcp_f32_e32 v186, v186
	s_nop 0
	v_mul_f32_e32 v184, v184, v186
	v_mul_f32_e32 v186, v185, v184
	v_add_f32_e32 v184, v126, v134
	v_min_f32_e32 v184, 0x40e00000, v184
	v_mul_f32_e32 v187, 0xc01d265f, v184
	v_exp_f32_e32 v187, v187
	v_add_f32_e32 v185, v94, v138
	v_med3_f32 v185, v185, s81, v222
	v_add_f32_e32 v185, 1.0, v185
	v_add_f32_e32 v187, 1.0, v187
	v_rcp_f32_e32 v187, v187
	s_nop 0
	v_mul_f32_e32 v184, v184, v187
	v_mul_f32_e32 v187, v185, v184
	v_add_f32_e32 v184, v127, v135
	v_min_f32_e32 v184, 0x40e00000, v184
	v_mul_f32_e32 v188, 0xc01d265f, v184
	v_exp_f32_e32 v188, v188
	v_add_f32_e32 v185, v95, v139
	v_med3_f32 v185, v185, s81, v222
	v_add_f32_e32 v185, 1.0, v185
	v_add_f32_e32 v188, 1.0, v188
	v_rcp_f32_e32 v188, v188
	s_nop 0
	v_mul_f32_e32 v184, v184, v188
	v_mul_f32_e32 v189, v185, v184
	v_cvt_pk_bf16_f32 v184, v2, v153
	v_add_f32_e32 v2, v120, v140
	v_min_f32_e32 v2, 0x40e00000, v2
	v_cvt_pk_bf16_f32 v185, v155, v182
	v_mul_f32_e32 v155, 0xc01d265f, v2
	v_exp_f32_e32 v155, v155
	v_add_u32_e32 v188, s48, v169
	v_add_f32_e32 v153, v88, v144
	v_cvt_pk_bf16_f32 v186, v183, v186
	v_add_f32_e32 v155, 1.0, v155
	v_rcp_f32_e32 v155, v155
	v_cvt_pk_bf16_f32 v187, v187, v189
	v_ashrrev_i32_e32 v189, 31, v188
	v_med3_f32 v153, v153, s81, v222
	v_lshlrev_b64 v[182:183], 11, v[188:189]
	v_mul_f32_e32 v2, v2, v155
	v_add_f32_e32 v153, 1.0, v153
	v_lshl_add_u64 v[182:183], s[90:91], 0, v[182:183]
	v_mul_f32_e32 v2, v153, v2
	v_add_f32_e32 v153, v121, v141
	v_lshl_add_u64 v[182:183], v[182:183], 0, v[160:161]
	v_min_f32_e32 v153, 0x40e00000, v153
	global_store_dwordx4 v[182:183], v[184:187], off
	v_mul_f32_e32 v182, 0xc01d265f, v153
	v_exp_f32_e32 v182, v182
	v_add_f32_e32 v155, v89, v145
	v_med3_f32 v155, v155, s81, v222
	v_add_f32_e32 v155, 1.0, v155
	v_add_f32_e32 v182, 1.0, v182
	v_rcp_f32_e32 v182, v182
	s_nop 0
	v_mul_f32_e32 v153, v153, v182
	v_mul_f32_e32 v153, v155, v153
	v_add_f32_e32 v155, v122, v142
	v_min_f32_e32 v155, 0x40e00000, v155
	v_mul_f32_e32 v183, 0xc01d265f, v155
	v_exp_f32_e32 v183, v183
	v_add_f32_e32 v182, v90, v146
	v_med3_f32 v182, v182, s81, v222
	v_add_f32_e32 v182, 1.0, v182
	v_add_f32_e32 v183, 1.0, v183
	v_rcp_f32_e32 v183, v183
	s_nop 0
	v_mul_f32_e32 v155, v155, v183
	v_mul_f32_e32 v155, v182, v155
	v_add_f32_e32 v182, v123, v143
	v_min_f32_e32 v182, 0x40e00000, v182
	v_mul_f32_e32 v184, 0xc01d265f, v182
	v_exp_f32_e32 v184, v184
	v_add_f32_e32 v183, v91, v147
	v_med3_f32 v183, v183, s81, v222
	v_add_f32_e32 v183, 1.0, v183
	v_add_f32_e32 v184, 1.0, v184
	v_rcp_f32_e32 v184, v184
	s_nop 0
	v_mul_f32_e32 v182, v182, v184
	v_mul_f32_e32 v183, v183, v182
	v_add_f32_e32 v182, v116, v132
	v_min_f32_e32 v182, 0x40e00000, v182
	v_mul_f32_e32 v185, 0xc01d265f, v182
	v_exp_f32_e32 v185, v185
	v_add_f32_e32 v184, v84, v136
	v_med3_f32 v184, v184, s81, v222
	v_add_f32_e32 v184, 1.0, v184
	v_add_f32_e32 v185, 1.0, v185
	v_rcp_f32_e32 v185, v185
	s_nop 0
	v_mul_f32_e32 v182, v182, v185
	v_mul_f32_e32 v184, v184, v182
	v_add_f32_e32 v182, v117, v133
	v_min_f32_e32 v182, 0x40e00000, v182
	v_mul_f32_e32 v186, 0xc01d265f, v182
	v_exp_f32_e32 v186, v186
	v_add_f32_e32 v185, v85, v137
	v_med3_f32 v185, v185, s81, v222
	v_add_f32_e32 v185, 1.0, v185
	v_add_f32_e32 v186, 1.0, v186
	v_rcp_f32_e32 v186, v186
	s_nop 0
	v_mul_f32_e32 v182, v182, v186
	v_mul_f32_e32 v185, v185, v182
	v_add_f32_e32 v182, v118, v134
	v_min_f32_e32 v182, 0x40e00000, v182
	v_mul_f32_e32 v187, 0xc01d265f, v182
	v_exp_f32_e32 v187, v187
	v_add_f32_e32 v186, v86, v138
	v_med3_f32 v186, v186, s81, v222
	v_add_f32_e32 v186, 1.0, v186
; __device__ __forceinline__ unsigned cvt_pk_bf16(float lo, float hi) { unsigned r; asm volatile("v_cvt_pk_bf16_f32 %0, %1, %2" : "=v"(r) : "v"(lo), "v"(hi)); return r; }
;     __device__ __forceinline__ void operator()(const pg8::f32x4 (&acc)[2][2][4][2], const pg8::Unit& u, int wr, int wc, int fr, int fq) const {
;     ...
;             for (int m = 0; m < 4; ++m) {
;                 const int row = u.pm + ai * 128 + wr * 64 + m * 16 + fr;
;                 float a[8];
; #pragma unroll
;                 for (int n = 0; n < 2; ++n)
; #pragma unroll
;                     for (int j = 0; j < 4; ++j) {
;                         const float g = fminf(acc[ai][0][m][n][j] + bgv[n][j], 7.f);
;                         const float l = fminf(fmaxf(acc[ai][1][m][n][j] + blv[n][j], -7.f), 7.f);
;                         const float sg = __builtin_amdgcn_rcpf(1.f + __builtin_amdgcn_exp2f(-1.702f * 1.4426950408889634f * g));
;                         a[n * 4 + j] = g * sg * (l + 1.f);
;                     }
;                 pg8::u32x4 w; w.x = pg8::cvt_pk_bf16(a[0], a[1]); w.y = pg8::cvt_pk_bf16(a[2], a[3]); w.z = pg8::cvt_pk_bf16(a[4], a[5]); w.w = pg8::cvt_pk_bf16(a[6], a[7]);
	v_add_f32_e32 v187, 1.0, v187
	v_rcp_f32_e32 v187, v187
	s_nop 0
	v_mul_f32_e32 v182, v182, v187
	v_mul_f32_e32 v187, v186, v182
	v_add_f32_e32 v182, v119, v135
	v_min_f32_e32 v182, 0x40e00000, v182
	v_mul_f32_e32 v188, 0xc01d265f, v182
	v_exp_f32_e32 v188, v188
	v_add_f32_e32 v186, v87, v139
	v_med3_f32 v186, v186, s81, v222
	v_add_f32_e32 v186, 1.0, v186
	v_add_f32_e32 v188, 1.0, v188
	v_rcp_f32_e32 v188, v188
	s_nop 0
	v_mul_f32_e32 v182, v182, v188
	v_mul_f32_e32 v188, v186, v182
	v_cvt_pk_bf16_f32 v182, v2, v153
	v_add_f32_e32 v2, v112, v140
	v_min_f32_e32 v2, 0x40e00000, v2
	v_cvt_pk_bf16_f32 v183, v155, v183
	v_mul_f32_e32 v155, 0xc01d265f, v2
	v_exp_f32_e32 v155, v155
	v_add_u32_e32 v186, s48, v151
	v_add_f32_e32 v153, v80, v144
	v_cvt_pk_bf16_f32 v184, v184, v185
	v_add_f32_e32 v155, 1.0, v155
	v_rcp_f32_e32 v155, v155
	v_cvt_pk_bf16_f32 v185, v187, v188
	v_ashrrev_i32_e32 v187, 31, v186
	v_med3_f32 v153, v153, s81, v222
	v_lshlrev_b64 v[186:187], 11, v[186:187]
	v_mul_f32_e32 v2, v2, v155
	v_add_f32_e32 v153, 1.0, v153
	v_lshl_add_u64 v[186:187], s[90:91], 0, v[186:187]
	v_mul_f32_e32 v2, v153, v2
	v_add_f32_e32 v153, v113, v141
	v_lshl_add_u64 v[186:187], v[186:187], 0, v[160:161]
	v_min_f32_e32 v153, 0x40e00000, v153
	global_store_dwordx4 v[186:187], v[182:185], off
	v_add_f32_e32 v155, v81, v145
	v_med3_f32 v155, v155, s81, v222
	v_mul_f32_e32 v182, 0xc01d265f, v153
	v_exp_f32_e32 v182, v182
	v_add_f32_e32 v155, 1.0, v155
	v_add_f32_e32 v182, 1.0, v182
	v_rcp_f32_e32 v182, v182
	s_nop 0
	v_mul_f32_e32 v153, v153, v182
	v_mul_f32_e32 v153, v155, v153
	v_add_f32_e32 v155, v114, v142
	v_min_f32_e32 v155, 0x40e00000, v155
	v_mul_f32_e32 v183, 0xc01d265f, v155
	v_exp_f32_e32 v183, v183
	v_add_f32_e32 v182, v82, v146
	v_med3_f32 v182, v182, s81, v222
	v_add_f32_e32 v182, 1.0, v182
	v_add_f32_e32 v183, 1.0, v183
	v_rcp_f32_e32 v183, v183
	s_nop 0
	v_mul_f32_e32 v155, v155, v183
	v_mul_f32_e32 v155, v182, v155
	v_add_f32_e32 v182, v115, v143
	v_min_f32_e32 v182, 0x40e00000, v182
	v_mul_f32_e32 v184, 0xc01d265f, v182
	v_exp_f32_e32 v184, v184
	v_add_f32_e32 v183, v83, v147
	v_med3_f32 v183, v183, s81, v222
	v_add_f32_e32 v183, 1.0, v183
	v_add_f32_e32 v184, 1.0, v184
	v_rcp_f32_e32 v184, v184
	s_nop 0
	v_mul_f32_e32 v182, v182, v184
	v_mul_f32_e32 v183, v183, v182
	v_add_f32_e32 v182, v108, v132
	v_min_f32_e32 v182, 0x40e00000, v182
	v_mul_f32_e32 v185, 0xc01d265f, v182
	v_exp_f32_e32 v185, v185
	v_add_f32_e32 v184, v76, v136
	v_med3_f32 v184, v184, s81, v222
	v_add_f32_e32 v184, 1.0, v184
	v_add_f32_e32 v185, 1.0, v185
	v_rcp_f32_e32 v185, v185
	s_nop 0
	v_mul_f32_e32 v182, v182, v185
	v_mul_f32_e32 v184, v184, v182
	v_add_f32_e32 v182, v109, v133
	v_min_f32_e32 v182, 0x40e00000, v182
	v_mul_f32_e32 v186, 0xc01d265f, v182
	v_exp_f32_e32 v186, v186
	v_add_f32_e32 v185, v77, v137
	v_med3_f32 v185, v185, s81, v222
	v_add_f32_e32 v185, 1.0, v185
	v_add_f32_e32 v186, 1.0, v186
	v_rcp_f32_e32 v186, v186
	s_nop 0
	v_mul_f32_e32 v182, v182, v186
	v_mul_f32_e32 v185, v185, v182
	v_add_f32_e32 v182, v110, v134
	v_min_f32_e32 v182, 0x40e00000, v182
	v_mul_f32_e32 v187, 0xc01d265f, v182
	v_exp_f32_e32 v187, v187
	v_add_f32_e32 v186, v78, v138
	v_med3_f32 v186, v186, s81, v222
	v_add_f32_e32 v186, 1.0, v186
	v_add_f32_e32 v187, 1.0, v187
	v_rcp_f32_e32 v187, v187
	s_nop 0
	v_mul_f32_e32 v182, v182, v187
	v_mul_f32_e32 v187, v186, v182
	v_add_f32_e32 v182, v111, v135
	v_min_f32_e32 v182, 0x40e00000, v182
	v_mul_f32_e32 v188, 0xc01d265f, v182
	v_exp_f32_e32 v188, v188
	v_add_f32_e32 v186, v79, v139
	v_med3_f32 v186, v186, s81, v222
	v_add_f32_e32 v186, 1.0, v186
	v_add_f32_e32 v188, 1.0, v188
	v_rcp_f32_e32 v188, v188
	s_nop 0
	v_mul_f32_e32 v182, v182, v188
	v_mul_f32_e32 v188, v186, v182
	v_cvt_pk_bf16_f32 v182, v2, v153
	v_add_f32_e32 v2, v104, v140
	v_min_f32_e32 v2, 0x40e00000, v2
	v_cvt_pk_bf16_f32 v183, v155, v183
	v_mul_f32_e32 v155, 0xc01d265f, v2
	v_exp_f32_e32 v155, v155
	v_add_u32_e32 v186, s48, v171
	v_add_f32_e32 v153, v72, v144
	v_cvt_pk_bf16_f32 v184, v184, v185
	v_add_f32_e32 v155, 1.0, v155
	v_rcp_f32_e32 v155, v155
	v_cvt_pk_bf16_f32 v185, v187, v188
	v_ashrrev_i32_e32 v187, 31, v186
	v_med3_f32 v153, v153, s81, v222
	v_lshlrev_b64 v[186:187], 11, v[186:187]
	v_mul_f32_e32 v2, v2, v155
	v_add_f32_e32 v153, 1.0, v153
	v_lshl_add_u64 v[186:187], s[90:91], 0, v[186:187]
	v_mul_f32_e32 v2, v153, v2
	v_add_f32_e32 v153, v105, v141
	v_lshl_add_u64 v[186:187], v[186:187], 0, v[160:161]
	v_min_f32_e32 v153, 0x40e00000, v153
	global_store_dwordx4 v[186:187], v[182:185], off
	v_add_f32_e32 v155, v73, v145
	v_med3_f32 v155, v155, s81, v222
	v_mul_f32_e32 v182, 0xc01d265f, v153
	v_exp_f32_e32 v182, v182
	v_add_f32_e32 v155, 1.0, v155
	v_add_f32_e32 v182, 1.0, v182
	v_rcp_f32_e32 v182, v182
	s_nop 0
	v_mul_f32_e32 v153, v153, v182
	v_mul_f32_e32 v153, v155, v153
	v_add_f32_e32 v155, v106, v142
	v_min_f32_e32 v155, 0x40e00000, v155
	v_mul_f32_e32 v183, 0xc01d265f, v155
	v_exp_f32_e32 v183, v183
	v_add_f32_e32 v182, v74, v146
	v_med3_f32 v182, v182, s81, v222
	v_add_f32_e32 v182, 1.0, v182
	v_add_f32_e32 v183, 1.0, v183
	v_rcp_f32_e32 v183, v183
	s_nop 0
	v_mul_f32_e32 v155, v155, v183
	v_mul_f32_e32 v155, v182, v155
	v_add_f32_e32 v182, v107, v143
	v_min_f32_e32 v182, 0x40e00000, v182
	v_mul_f32_e32 v184, 0xc01d265f, v182
	v_exp_f32_e32 v184, v184
	v_add_f32_e32 v183, v75, v147
	v_med3_f32 v183, v183, s81, v222
	v_add_f32_e32 v183, 1.0, v183
	v_add_f32_e32 v184, 1.0, v184
	v_rcp_f32_e32 v184, v184
	s_nop 0
	v_mul_f32_e32 v182, v182, v184
	v_mul_f32_e32 v183, v183, v182
	v_add_f32_e32 v182, v100, v132
	v_min_f32_e32 v182, 0x40e00000, v182
; __device__ __forceinline__ unsigned cvt_pk_bf16(float lo, float hi) { unsigned r; asm volatile("v_cvt_pk_bf16_f32 %0, %1, %2" : "=v"(r) : "v"(lo), "v"(hi)); return r; }
;     __device__ __forceinline__ void operator()(const pg8::f32x4 (&acc)[2][2][4][2], const pg8::Unit& u, int wr, int wc, int fr, int fq) const {
;     ...
;             for (int m = 0; m < 4; ++m) {
;                 const int row = u.pm + ai * 128 + wr * 64 + m * 16 + fr;
;                 float a[8];
; #pragma unroll
;                 for (int n = 0; n < 2; ++n)
; #pragma unroll
;                     for (int j = 0; j < 4; ++j) {
;                         const float g = fminf(acc[ai][0][m][n][j] + bgv[n][j], 7.f);
;                         const float l = fminf(fmaxf(acc[ai][1][m][n][j] + blv[n][j], -7.f), 7.f);
;                         const float sg = __builtin_amdgcn_rcpf(1.f + __builtin_amdgcn_exp2f(-1.702f * 1.4426950408889634f * g));
;                         a[n * 4 + j] = g * sg * (l + 1.f);
;                     }
;                 pg8::u32x4 w; w.x = pg8::cvt_pk_bf16(a[0], a[1]); w.y = pg8::cvt_pk_bf16(a[2], a[3]); w.z = pg8::cvt_pk_bf16(a[4], a[5]); w.w = pg8::cvt_pk_bf16(a[6], a[7]);
	v_mul_f32_e32 v185, 0xc01d265f, v182
	v_exp_f32_e32 v185, v185
	v_add_f32_e32 v184, v68, v136
	v_med3_f32 v184, v184, s81, v222
	v_add_f32_e32 v184, 1.0, v184
	v_add_f32_e32 v185, 1.0, v185
	v_rcp_f32_e32 v185, v185
	s_nop 0
	v_mul_f32_e32 v182, v182, v185
	v_mul_f32_e32 v184, v184, v182
	v_add_f32_e32 v182, v101, v133
	v_min_f32_e32 v182, 0x40e00000, v182
	v_mul_f32_e32 v186, 0xc01d265f, v182
	v_exp_f32_e32 v186, v186
	v_add_f32_e32 v185, v69, v137
	v_med3_f32 v185, v185, s81, v222
	v_add_f32_e32 v185, 1.0, v185
	v_add_f32_e32 v186, 1.0, v186
	v_rcp_f32_e32 v186, v186
	s_nop 0
	v_mul_f32_e32 v182, v182, v186
	v_mul_f32_e32 v185, v185, v182
	v_add_f32_e32 v182, v102, v134
	v_min_f32_e32 v182, 0x40e00000, v182
	v_mul_f32_e32 v187, 0xc01d265f, v182
	v_exp_f32_e32 v187, v187
	v_add_f32_e32 v186, v70, v138
	v_med3_f32 v186, v186, s81, v222
	v_add_f32_e32 v186, 1.0, v186
	v_add_f32_e32 v187, 1.0, v187
	v_rcp_f32_e32 v187, v187
	s_nop 0
	v_mul_f32_e32 v182, v182, v187
	v_mul_f32_e32 v187, v186, v182
	v_add_f32_e32 v182, v103, v135
	v_min_f32_e32 v182, 0x40e00000, v182
	v_mul_f32_e32 v188, 0xc01d265f, v182
	v_exp_f32_e32 v188, v188
	v_add_f32_e32 v186, v71, v139
	v_med3_f32 v186, v186, s81, v222
	v_add_f32_e32 v186, 1.0, v186
	v_add_f32_e32 v188, 1.0, v188
	v_rcp_f32_e32 v188, v188
	s_nop 0
	v_mul_f32_e32 v182, v182, v188
	v_mul_f32_e32 v188, v186, v182
	v_cvt_pk_bf16_f32 v182, v2, v153
	v_add_f32_e32 v2, v64, v140
	v_min_f32_e32 v2, 0x40e00000, v2
	v_cvt_pk_bf16_f32 v183, v155, v183
	v_mul_f32_e32 v155, 0xc01d265f, v2
	v_exp_f32_e32 v155, v155
	v_add_u32_e32 v186, s48, v172
	v_add_f32_e32 v153, v32, v144
	v_cvt_pk_bf16_f32 v184, v184, v185
	v_add_f32_e32 v155, 1.0, v155
	v_rcp_f32_e32 v155, v155
	v_cvt_pk_bf16_f32 v185, v187, v188
	v_ashrrev_i32_e32 v187, 31, v186
	v_med3_f32 v153, v153, s81, v222
	v_lshlrev_b64 v[186:187], 11, v[186:187]
	v_mul_f32_e32 v2, v2, v155
	v_add_f32_e32 v153, 1.0, v153
	v_lshl_add_u64 v[186:187], s[90:91], 0, v[186:187]
	v_mul_f32_e32 v2, v153, v2
	v_add_f32_e32 v153, v65, v141
	v_lshl_add_u64 v[186:187], v[186:187], 0, v[160:161]
	v_min_f32_e32 v153, 0x40e00000, v153
	global_store_dwordx4 v[186:187], v[182:185], off
	v_add_f32_e32 v155, v33, v145
	v_med3_f32 v155, v155, s81, v222
	v_mul_f32_e32 v182, 0xc01d265f, v153
	v_exp_f32_e32 v182, v182
	v_add_f32_e32 v155, 1.0, v155
	v_add_f32_e32 v182, 1.0, v182
	v_rcp_f32_e32 v182, v182
	s_nop 0
	v_mul_f32_e32 v153, v153, v182
	v_mul_f32_e32 v153, v155, v153
	v_add_f32_e32 v155, v66, v142
	v_min_f32_e32 v155, 0x40e00000, v155
	v_mul_f32_e32 v183, 0xc01d265f, v155
	v_exp_f32_e32 v183, v183
	v_add_f32_e32 v182, v34, v146
	v_med3_f32 v182, v182, s81, v222
	v_add_f32_e32 v182, 1.0, v182
	v_add_f32_e32 v183, 1.0, v183
	v_rcp_f32_e32 v183, v183
	s_nop 0
	v_mul_f32_e32 v155, v155, v183
	v_mul_f32_e32 v155, v182, v155
	v_add_f32_e32 v182, v67, v143
	v_min_f32_e32 v182, 0x40e00000, v182
	v_mul_f32_e32 v184, 0xc01d265f, v182
	v_exp_f32_e32 v184, v184
	v_add_f32_e32 v183, v35, v147
	v_med3_f32 v183, v183, s81, v222
	v_add_f32_e32 v183, 1.0, v183
	v_add_f32_e32 v184, 1.0, v184
	v_rcp_f32_e32 v184, v184
	s_nop 0
	v_mul_f32_e32 v182, v182, v184
	v_mul_f32_e32 v183, v183, v182
	v_add_f32_e32 v182, v60, v132
	v_min_f32_e32 v182, 0x40e00000, v182
	v_mul_f32_e32 v185, 0xc01d265f, v182
	v_exp_f32_e32 v185, v185
	v_add_f32_e32 v184, v28, v136
	v_med3_f32 v184, v184, s81, v222
	v_add_f32_e32 v184, 1.0, v184
	v_add_f32_e32 v185, 1.0, v185
	v_rcp_f32_e32 v185, v185
	s_nop 0
	v_mul_f32_e32 v182, v182, v185
	v_mul_f32_e32 v184, v184, v182
	v_add_f32_e32 v182, v61, v133
	v_min_f32_e32 v182, 0x40e00000, v182
	v_mul_f32_e32 v186, 0xc01d265f, v182
	v_exp_f32_e32 v186, v186
	v_add_f32_e32 v185, v29, v137
	v_med3_f32 v185, v185, s81, v222
	v_add_f32_e32 v185, 1.0, v185
	v_add_f32_e32 v186, 1.0, v186
	v_rcp_f32_e32 v186, v186
	s_nop 0
	v_mul_f32_e32 v182, v182, v186
	v_mul_f32_e32 v185, v185, v182
	v_add_f32_e32 v182, v62, v134
	v_min_f32_e32 v182, 0x40e00000, v182
	v_mul_f32_e32 v187, 0xc01d265f, v182
	v_exp_f32_e32 v187, v187
	v_add_f32_e32 v186, v30, v138
	v_med3_f32 v186, v186, s81, v222
	v_add_f32_e32 v186, 1.0, v186
	v_add_f32_e32 v187, 1.0, v187
	v_rcp_f32_e32 v187, v187
	s_nop 0
	v_mul_f32_e32 v182, v182, v187
	v_mul_f32_e32 v187, v186, v182
	v_add_f32_e32 v182, v63, v135
	v_min_f32_e32 v182, 0x40e00000, v182
	v_mul_f32_e32 v188, 0xc01d265f, v182
	v_exp_f32_e32 v188, v188
	v_add_f32_e32 v186, v31, v139
	v_med3_f32 v186, v186, s81, v222
	v_add_f32_e32 v186, 1.0, v186
	v_add_f32_e32 v188, 1.0, v188
	v_rcp_f32_e32 v188, v188
	s_nop 0
	v_mul_f32_e32 v182, v182, v188
	v_mul_f32_e32 v188, v186, v182
	v_cvt_pk_bf16_f32 v182, v2, v153
	v_add_f32_e32 v2, v56, v140
	v_min_f32_e32 v2, 0x40e00000, v2
	v_cvt_pk_bf16_f32 v183, v155, v183
	v_mul_f32_e32 v155, 0xc01d265f, v2
	v_exp_f32_e32 v155, v155
	v_add_u32_e32 v186, s48, v173
	v_add_f32_e32 v153, v24, v144
	v_cvt_pk_bf16_f32 v184, v184, v185
	v_add_f32_e32 v155, 1.0, v155
	v_rcp_f32_e32 v155, v155
	v_cvt_pk_bf16_f32 v185, v187, v188
	v_ashrrev_i32_e32 v187, 31, v186
	v_med3_f32 v153, v153, s81, v222
	v_lshlrev_b64 v[186:187], 11, v[186:187]
	v_mul_f32_e32 v2, v2, v155
	v_add_f32_e32 v153, 1.0, v153
	v_lshl_add_u64 v[186:187], s[90:91], 0, v[186:187]
	v_mul_f32_e32 v2, v153, v2
	v_add_f32_e32 v153, v57, v141
	v_lshl_add_u64 v[186:187], v[186:187], 0, v[160:161]
	v_min_f32_e32 v153, 0x40e00000, v153
	global_store_dwordx4 v[186:187], v[182:185], off
	v_add_f32_e32 v155, v25, v145
	v_med3_f32 v155, v155, s81, v222
	v_mul_f32_e32 v182, 0xc01d265f, v153
	v_exp_f32_e32 v182, v182
	v_add_f32_e32 v155, 1.0, v155
	v_add_f32_e32 v182, 1.0, v182
	v_rcp_f32_e32 v182, v182
; __device__ __forceinline__ unsigned cvt_pk_bf16(float lo, float hi) { unsigned r; asm volatile("v_cvt_pk_bf16_f32 %0, %1, %2" : "=v"(r) : "v"(lo), "v"(hi)); return r; }
;     __device__ __forceinline__ void operator()(const pg8::f32x4 (&acc)[2][2][4][2], const pg8::Unit& u, int wr, int wc, int fr, int fq) const {
;     ...
;             for (int m = 0; m < 4; ++m) {
;                 const int row = u.pm + ai * 128 + wr * 64 + m * 16 + fr;
;                 float a[8];
; #pragma unroll
;                 for (int n = 0; n < 2; ++n)
; #pragma unroll
;                     for (int j = 0; j < 4; ++j) {
;                         const float g = fminf(acc[ai][0][m][n][j] + bgv[n][j], 7.f);
;                         const float l = fminf(fmaxf(acc[ai][1][m][n][j] + blv[n][j], -7.f), 7.f);
;                         const float sg = __builtin_amdgcn_rcpf(1.f + __builtin_amdgcn_exp2f(-1.702f * 1.4426950408889634f * g));
;                         a[n * 4 + j] = g * sg * (l + 1.f);
;                     }
;                 pg8::u32x4 w; w.x = pg8::cvt_pk_bf16(a[0], a[1]); w.y = pg8::cvt_pk_bf16(a[2], a[3]); w.z = pg8::cvt_pk_bf16(a[4], a[5]); w.w = pg8::cvt_pk_bf16(a[6], a[7]);
	s_nop 0
	v_mul_f32_e32 v153, v153, v182
	v_mul_f32_e32 v153, v155, v153
	v_add_f32_e32 v155, v58, v142
	v_min_f32_e32 v155, 0x40e00000, v155
	v_mul_f32_e32 v183, 0xc01d265f, v155
	v_exp_f32_e32 v183, v183
	v_add_f32_e32 v182, v26, v146
	v_med3_f32 v182, v182, s81, v222
	v_add_f32_e32 v182, 1.0, v182
	v_add_f32_e32 v183, 1.0, v183
	v_rcp_f32_e32 v183, v183
	s_nop 0
	v_mul_f32_e32 v155, v155, v183
	v_mul_f32_e32 v155, v182, v155
	v_add_f32_e32 v182, v59, v143
	v_min_f32_e32 v182, 0x40e00000, v182
	v_mul_f32_e32 v184, 0xc01d265f, v182
	v_exp_f32_e32 v184, v184
	v_add_f32_e32 v183, v27, v147
	v_med3_f32 v183, v183, s81, v222
	v_add_f32_e32 v183, 1.0, v183
	v_add_f32_e32 v184, 1.0, v184
	v_rcp_f32_e32 v184, v184
	s_nop 0
	v_mul_f32_e32 v182, v182, v184
	v_mul_f32_e32 v183, v183, v182
	v_add_f32_e32 v182, v52, v132
	v_min_f32_e32 v182, 0x40e00000, v182
	v_mul_f32_e32 v185, 0xc01d265f, v182
	v_exp_f32_e32 v185, v185
	v_add_f32_e32 v184, v20, v136
	v_med3_f32 v184, v184, s81, v222
	v_add_f32_e32 v184, 1.0, v184
	v_add_f32_e32 v185, 1.0, v185
	v_rcp_f32_e32 v185, v185
	s_nop 0
	v_mul_f32_e32 v182, v182, v185
	v_mul_f32_e32 v184, v184, v182
	v_add_f32_e32 v182, v53, v133
	v_min_f32_e32 v182, 0x40e00000, v182
	v_mul_f32_e32 v186, 0xc01d265f, v182
	v_exp_f32_e32 v186, v186
	v_add_f32_e32 v185, v21, v137
	v_med3_f32 v185, v185, s81, v222
	v_add_f32_e32 v185, 1.0, v185
	v_add_f32_e32 v186, 1.0, v186
	v_rcp_f32_e32 v186, v186
	s_nop 0
	v_mul_f32_e32 v182, v182, v186
	v_mul_f32_e32 v185, v185, v182
	v_add_f32_e32 v182, v54, v134
	v_min_f32_e32 v182, 0x40e00000, v182
	v_mul_f32_e32 v187, 0xc01d265f, v182
	v_exp_f32_e32 v187, v187
	v_add_f32_e32 v186, v22, v138
	v_med3_f32 v186, v186, s81, v222
	v_add_f32_e32 v186, 1.0, v186
	v_add_f32_e32 v187, 1.0, v187
	v_rcp_f32_e32 v187, v187
	s_nop 0
	v_mul_f32_e32 v182, v182, v187
	v_mul_f32_e32 v187, v186, v182
	v_add_f32_e32 v182, v55, v135
	v_min_f32_e32 v182, 0x40e00000, v182
	v_mul_f32_e32 v188, 0xc01d265f, v182
	v_exp_f32_e32 v188, v188
	v_add_f32_e32 v186, v23, v139
	v_med3_f32 v186, v186, s81, v222
	v_add_f32_e32 v186, 1.0, v186
	v_add_f32_e32 v188, 1.0, v188
	v_rcp_f32_e32 v188, v188
	s_nop 0
	v_mul_f32_e32 v182, v182, v188
	v_mul_f32_e32 v188, v186, v182
	v_cvt_pk_bf16_f32 v182, v2, v153
	v_add_f32_e32 v2, v48, v140
	v_min_f32_e32 v2, 0x40e00000, v2
	v_cvt_pk_bf16_f32 v183, v155, v183
	v_mul_f32_e32 v155, 0xc01d265f, v2
	v_exp_f32_e32 v155, v155
	v_add_u32_e32 v186, s48, v174
	v_add_f32_e32 v153, v16, v144
	v_cvt_pk_bf16_f32 v184, v184, v185
	v_add_f32_e32 v155, 1.0, v155
	v_rcp_f32_e32 v155, v155
	v_cvt_pk_bf16_f32 v185, v187, v188
	v_ashrrev_i32_e32 v187, 31, v186
	v_med3_f32 v153, v153, s81, v222
	v_lshlrev_b64 v[186:187], 11, v[186:187]
	v_mul_f32_e32 v2, v2, v155
	v_add_f32_e32 v153, 1.0, v153
	v_lshl_add_u64 v[186:187], s[90:91], 0, v[186:187]
	v_mul_f32_e32 v2, v153, v2
	v_add_f32_e32 v153, v49, v141
	v_lshl_add_u64 v[186:187], v[186:187], 0, v[160:161]
	v_min_f32_e32 v153, 0x40e00000, v153
	global_store_dwordx4 v[186:187], v[182:185], off
	v_add_f32_e32 v155, v17, v145
	v_med3_f32 v155, v155, s81, v222
	v_mul_f32_e32 v182, 0xc01d265f, v153
	v_exp_f32_e32 v182, v182
	v_add_f32_e32 v155, 1.0, v155
	v_add_f32_e32 v182, 1.0, v182
	v_rcp_f32_e32 v182, v182
	s_nop 0
	v_mul_f32_e32 v153, v153, v182
	v_mul_f32_e32 v153, v155, v153
	v_add_f32_e32 v155, v50, v142
	v_min_f32_e32 v155, 0x40e00000, v155
	v_mul_f32_e32 v183, 0xc01d265f, v155
	v_exp_f32_e32 v183, v183
	v_add_f32_e32 v182, v18, v146
	v_med3_f32 v182, v182, s81, v222
	v_add_f32_e32 v182, 1.0, v182
	v_add_f32_e32 v183, 1.0, v183
	v_rcp_f32_e32 v183, v183
	s_nop 0
	v_mul_f32_e32 v155, v155, v183
	v_mul_f32_e32 v155, v182, v155
	v_add_f32_e32 v182, v51, v143
	v_min_f32_e32 v182, 0x40e00000, v182
	v_mul_f32_e32 v184, 0xc01d265f, v182
	v_exp_f32_e32 v184, v184
	v_add_f32_e32 v183, v19, v147
	v_med3_f32 v183, v183, s81, v222
	v_add_f32_e32 v183, 1.0, v183
	v_add_f32_e32 v184, 1.0, v184
	v_rcp_f32_e32 v184, v184
	s_nop 0
	v_mul_f32_e32 v182, v182, v184
	v_mul_f32_e32 v183, v183, v182
	v_add_f32_e32 v182, v44, v132
	v_min_f32_e32 v182, 0x40e00000, v182
	v_mul_f32_e32 v185, 0xc01d265f, v182
	v_exp_f32_e32 v185, v185
	v_add_f32_e32 v184, v12, v136
	v_med3_f32 v184, v184, s81, v222
	v_add_f32_e32 v184, 1.0, v184
	v_add_f32_e32 v185, 1.0, v185
	v_rcp_f32_e32 v185, v185
	v_add_f32_e32 v132, v36, v132
	v_min_f32_e32 v132, 0x40e00000, v132
	v_add_f32_e32 v136, v4, v136
	v_mul_f32_e32 v182, v182, v185
	v_mul_f32_e32 v184, v184, v182
	v_add_f32_e32 v182, v45, v133
	v_min_f32_e32 v182, 0x40e00000, v182
	v_mul_f32_e32 v186, 0xc01d265f, v182
; __device__ __forceinline__ unsigned cvt_pk_bf16(float lo, float hi) { unsigned r; asm volatile("v_cvt_pk_bf16_f32 %0, %1, %2" : "=v"(r) : "v"(lo), "v"(hi)); return r; }
; #define PG8_BAR __builtin_amdgcn_s_barrier()
; template <class Epi, class Sched, bool ALIGN_EPI = false, bool SP2 = false, bool GATHER = false, bool HALFM = false>
; __device__ __forceinline__ void gemm_phase(PG8_LAS unsigned char* lds, const int Kdim, const Sched& S, const Epi& E) {
;     ...
;         if (!has_next) break;
; #pragma unroll
;         for (int a = 0; a < 2; ++a)
; #pragma unroll
;             for (int b = 0; b < 2; ++b)
; #pragma unroll
;                 for (int m = 0; m < 4; ++m)
; #pragma unroll
;                     for (int n = 0; n < 2; ++n) acc[a][b][m][n] = (f32x4){0.f, 0.f, 0.f, 0.f};
;         cur = nxt; cA = nA; cB = nB; ++ui;
;         if constexpr (GATHER) {
; #pragma unroll
;             for (int h = 0; h < 2; ++h)
; #pragma unroll
;                 for (int i = 0; i < 2; ++i) { gc[h][i] = gn[h][i]; if (has_nn) gn[h][i] = (unsigned)ix[h][i] * (unsigned)(K * 2) + CA2[i]; } }
;         if constexpr (ALIGN_EPI) { if (wr == 1) PG8_BAR; }
;     __device__ __forceinline__ void operator()(const pg8::f32x4 (&acc)[2][2][4][2], const pg8::Unit& u, int wr, int wc, int fr, int fq) const {
;     ...
;             for (int m = 0; m < 4; ++m) {
;                 const int row = u.pm + ai * 128 + wr * 64 + m * 16 + fr;
;                 float a[8];
; #pragma unroll
;                 for (int n = 0; n < 2; ++n)
; #pragma unroll
;                     for (int j = 0; j < 4; ++j) {
;                         const float g = fminf(acc[ai][0][m][n][j] + bgv[n][j], 7.f);
;                         const float l = fminf(fmaxf(acc[ai][1][m][n][j] + blv[n][j], -7.f), 7.f);
;                         const float sg = __builtin_amdgcn_rcpf(1.f + __builtin_amdgcn_exp2f(-1.702f * 1.4426950408889634f * g));
;                         a[n * 4 + j] = g * sg * (l + 1.f);
;                     }
;                 pg8::u32x4 w; w.x = pg8::cvt_pk_bf16(a[0], a[1]); w.y = pg8::cvt_pk_bf16(a[2], a[3]); w.z = pg8::cvt_pk_bf16(a[4], a[5]); w.w = pg8::cvt_pk_bf16(a[6], a[7]);
;                 *(pg8::u32x4*)(ACT + (size_t)row * 1024 + colj) = w;
	v_exp_f32_e32 v186, v186
	v_add_f32_e32 v185, v13, v137
	v_med3_f32 v185, v185, s81, v222
	v_add_f32_e32 v185, 1.0, v185
	v_add_f32_e32 v186, 1.0, v186
	v_rcp_f32_e32 v186, v186
	v_med3_f32 v136, v136, s81, v222
	v_add_f32_e32 v136, 1.0, v136
	v_mul_f32_e32 v182, v182, v186
	v_mul_f32_e32 v185, v185, v182
	v_add_f32_e32 v182, v46, v134
	v_min_f32_e32 v182, 0x40e00000, v182
	v_mul_f32_e32 v187, 0xc01d265f, v182
	v_exp_f32_e32 v187, v187
	v_add_f32_e32 v186, v14, v138
	v_med3_f32 v186, v186, s81, v222
	v_add_f32_e32 v186, 1.0, v186
	v_add_f32_e32 v187, 1.0, v187
	v_rcp_f32_e32 v187, v187
	s_nop 0
	v_mul_f32_e32 v182, v182, v187
	v_mul_f32_e32 v187, v186, v182
	v_add_f32_e32 v182, v47, v135
	v_min_f32_e32 v182, 0x40e00000, v182
	v_mul_f32_e32 v188, 0xc01d265f, v182
	v_exp_f32_e32 v188, v188
	v_add_f32_e32 v186, v15, v139
	v_med3_f32 v186, v186, s81, v222
	v_add_f32_e32 v186, 1.0, v186
	v_add_f32_e32 v188, 1.0, v188
	v_rcp_f32_e32 v188, v188
	s_nop 0
	v_mul_f32_e32 v182, v182, v188
	v_mul_f32_e32 v188, v186, v182
	v_cvt_pk_bf16_f32 v182, v2, v153
	v_add_f32_e32 v2, v40, v140
	v_min_f32_e32 v2, 0x40e00000, v2
	v_add_f32_e32 v140, v8, v144
	v_mul_f32_e32 v144, 0xc01d265f, v2
	v_exp_f32_e32 v144, v144
	v_med3_f32 v140, v140, s81, v222
	v_add_f32_e32 v140, 1.0, v140
	v_add_u32_e32 v186, s48, v175
	v_add_f32_e32 v144, 1.0, v144
	v_rcp_f32_e32 v144, v144
	v_cvt_pk_bf16_f32 v183, v155, v183
	v_cvt_pk_bf16_f32 v184, v184, v185
	v_cvt_pk_bf16_f32 v185, v187, v188
	v_ashrrev_i32_e32 v187, 31, v186
	v_mul_f32_e32 v2, v2, v144
	v_mul_f32_e32 v2, v140, v2
	v_add_f32_e32 v140, v41, v141
	v_min_f32_e32 v140, 0x40e00000, v140
	v_mul_f32_e32 v144, 0xc01d265f, v140
	v_exp_f32_e32 v144, v144
	v_add_f32_e32 v141, v9, v145
	v_med3_f32 v141, v141, s81, v222
	v_add_f32_e32 v141, 1.0, v141
	v_add_f32_e32 v144, 1.0, v144
	v_rcp_f32_e32 v144, v144
	v_lshlrev_b64 v[186:187], 11, v[186:187]
	v_lshl_add_u64 v[186:187], s[90:91], 0, v[186:187]
	v_lshl_add_u64 v[186:187], v[186:187], 0, v[160:161]
	v_mul_f32_e32 v140, v140, v144
	v_mul_f32_e32 v140, v141, v140
	v_add_f32_e32 v141, v42, v142
	v_min_f32_e32 v141, 0x40e00000, v141
	v_mul_f32_e32 v144, 0xc01d265f, v141
	v_exp_f32_e32 v144, v144
	v_add_f32_e32 v142, v10, v146
	v_med3_f32 v142, v142, s81, v222
	v_add_f32_e32 v142, 1.0, v142
	v_add_f32_e32 v144, 1.0, v144
	v_rcp_f32_e32 v144, v144
	global_store_dwordx4 v[186:187], v[182:185], off
	v_mul_f32_e32 v141, v141, v144
	v_mul_f32_e32 v141, v142, v141
	v_add_f32_e32 v142, v43, v143
	v_min_f32_e32 v142, 0x40e00000, v142
	v_mul_f32_e32 v144, 0xc01d265f, v142
	v_exp_f32_e32 v144, v144
	v_add_f32_e32 v143, v11, v147
	v_med3_f32 v143, v143, s81, v222
	v_add_f32_e32 v143, 1.0, v143
	v_add_f32_e32 v144, 1.0, v144
	v_rcp_f32_e32 v144, v144
	s_nop 0
	v_mul_f32_e32 v142, v142, v144
	v_mul_f32_e32 v142, v143, v142
	v_mul_f32_e32 v143, 0xc01d265f, v132
	v_exp_f32_e32 v143, v143
	s_nop 0
	v_add_f32_e32 v143, 1.0, v143
	v_rcp_f32_e32 v143, v143
	s_nop 0
	v_mul_f32_e32 v132, v132, v143
	v_mul_f32_e32 v143, v136, v132
	v_add_f32_e32 v132, v37, v133
	v_min_f32_e32 v132, 0x40e00000, v132
	v_mul_f32_e32 v136, 0xc01d265f, v132
	v_exp_f32_e32 v136, v136
	v_add_f32_e32 v133, v5, v137
	v_med3_f32 v133, v133, s81, v222
	v_add_f32_e32 v133, 1.0, v133
	v_add_f32_e32 v136, 1.0, v136
	v_rcp_f32_e32 v136, v136
	s_nop 0
	v_mul_f32_e32 v132, v132, v136
	v_mul_f32_e32 v137, v133, v132
	v_add_f32_e32 v132, v38, v134
	v_min_f32_e32 v132, 0x40e00000, v132
	v_mul_f32_e32 v134, 0xc01d265f, v132
	v_exp_f32_e32 v134, v134
	v_add_f32_e32 v133, v6, v138
	v_med3_f32 v133, v133, s81, v222
	v_add_f32_e32 v133, 1.0, v133
	v_add_f32_e32 v134, 1.0, v134
	v_rcp_f32_e32 v134, v134
	v_add_u32_e32 v136, s48, v176
	v_mul_f32_e32 v132, v132, v134
	v_mul_f32_e32 v138, v133, v132
	v_add_f32_e32 v132, v39, v135
	v_min_f32_e32 v132, 0x40e00000, v132
	v_mul_f32_e32 v134, 0xc01d265f, v132
	v_exp_f32_e32 v134, v134
	v_add_f32_e32 v133, v7, v139
	v_med3_f32 v133, v133, s81, v222
	v_add_f32_e32 v133, 1.0, v133
	v_add_f32_e32 v134, 1.0, v134
	v_rcp_f32_e32 v134, v134
	s_nop 0
	v_mul_f32_e32 v132, v132, v134
	v_mul_f32_e32 v135, v133, v132
	v_cvt_pk_bf16_f32 v132, v2, v140
	v_cvt_pk_bf16_f32 v133, v141, v142
	v_cvt_pk_bf16_f32 v134, v143, v137
	v_ashrrev_i32_e32 v137, 31, v136
	v_lshlrev_b64 v[136:137], 11, v[136:137]
	v_lshl_add_u64 v[136:137], s[90:91], 0, v[136:137]
	v_lshl_add_u64 v[136:137], v[136:137], 0, v[160:161]
	v_cvt_pk_bf16_f32 v135, v138, v135
	global_store_dwordx4 v[136:137], v[132:135], off
	s_cbranch_vccnz .LBB0_1722
	v_readlane_b32 s82, v255, 1
	v_readlane_b32 s83, v255, 2
	s_branch .LBB0_1697

; #define PG8_STAGE(bufoff, gbase, voff) do { _Pragma("unroll") for (int _i = 0; _i < 2; ++_i) \
;         __builtin_amdgcn_global_load_lds((const unsigned*)((const char*)(gbase) + (voff)[_i]), (PG8_LAS unsigned*)(lds + (bufoff) + ldsw + _i * 8192), 16, 0, 0); } while (0)
; #define PG8_STAGE_G(bufoff, kb, g) do { _Pragma("unroll") for (int _i = 0; _i < 2; ++_i) \
;         __builtin_amdgcn_global_load_lds((const unsigned*)(gA + (size_t)(kb) + (g)[_i]), (PG8_LAS unsigned*)(lds + (bufoff) + ldsw + _i * 8192), 16, 0, 0); } while (0)
; #define PG8_LDA(dst, b, h) do { _Pragma("unroll") for (int m = 0; m < 4; ++m) _Pragma("unroll") for (int k = 0; k < 2; ++k) dst[m][k] = *(const PG8_LAS bf16x8*)(lds + PG8_SA(b, h) + aoff + m * 2048 + k * 1024); } while (0)
; #define PG8_LDB(dst, b, h) do { _Pragma("unroll") for (int n = 0; n < 2; ++n) _Pragma("unroll") for (int k = 0; k < 2; ++k) dst[n][k] = *(const PG8_LAS bf16x8*)(lds + PG8_SB(b, h) + boff + n * 2048 + k * 1024); } while (0)
; #define PG8_WAIT_V(n) asm volatile("s_waitcnt vmcnt(" #n ")" ::: "memory")
; #define PG8_WAIT_L(n) asm volatile("s_waitcnt lgkmcnt(" #n ")" ::: "memory")
; template <class Epi, class Sched, bool ALIGN_EPI = false, bool SP2 = false, bool GATHER = false, bool HALFM = false>
; __device__ __forceinline__ void gemm_phase(PG8_LAS unsigned char* lds, const int Kdim, const Sched& S, const Epi& E) {
;     ...
;             PG8_LDB(B0, 0, 0); PG8_LDB(B1, 0, 1); PG8_SCHED; PG8_LDA(At, 0, 0); if constexpr (GATHER) PG8_STAGE_G(PG8_SA(1, 1), (size_t)(t + 1) * kstep, gc[1]); else PG8_STAGE(PG8_SA(1, 1), a1 + hstep, voffA);
;             PG8_WAIT_V(8); PG8_WAIT_L(0); PG8_BAR; PG8_MMA(0, 0, At, B0); PG8_MMA(0, 1, At, B1); PG8_BAR; PG8_SCHED;
;     ...
; #pragma unroll
;         for (int a = 0; a < 2; ++a)
; #pragma unroll
;             for (int b = 0; b < 2; ++b)
; #pragma unroll
;                 for (int m = 0; m < 4; ++m)
; #pragma unroll
;                     for (int n = 0; n < 2; ++n) acc[a][b][m][n] = (f32x4){0.f, 0.f, 0.f, 0.f};
;         cur = nxt; cA = nA; cB = nB; ++ui;
;         if constexpr (GATHER) {
; #pragma unroll
;             for (int h = 0; h < 2; ++h)
; #pragma unroll
;                 for (int i = 0; i < 2; ++i) { gc[h][i] = gn[h][i]; if (has_nn) gn[h][i] = (unsigned)ix[h][i] * (unsigned)(K * 2) + CA2[i]; } }
;         if constexpr (ALIGN_EPI) { if (wr == 1) PG8_BAR; }
.LBB0_1816:
	s_and_b64 s[20:21], s[42:43], exec
	s_cselect_b32 s17, s39, s5
	s_cselect_b32 s36, s38, s4
	s_cselect_b32 s53, s41, s25
	s_cselect_b32 s54, s40, s24
	s_add_u32 s44, s4, 0x40080
	s_addc_u32 s45, s5, 0
	s_add_u32 s55, s24, 0x100
	v_mov_b32_e32 v4, 0
	s_addc_u32 s56, s25, 0
	s_mov_b32 s57, -2
	v_mov_b32_e32 v5, v4
	v_mov_b32_e32 v6, v4
	v_mov_b32_e32 v7, v4
	v_mov_b32_e32 v8, v4
	v_mov_b32_e32 v9, v4
	v_mov_b32_e32 v10, v4
	v_mov_b32_e32 v11, v4
	v_mov_b32_e32 v16, v4
	v_mov_b32_e32 v17, v4
	v_mov_b32_e32 v18, v4
	v_mov_b32_e32 v19, v4
	v_mov_b32_e32 v24, v4
	v_mov_b32_e32 v25, v4
	v_mov_b32_e32 v26, v4
	v_mov_b32_e32 v27, v4
	v_mov_b32_e32 v32, v4
	v_mov_b32_e32 v33, v4
	v_mov_b32_e32 v34, v4
	v_mov_b32_e32 v35, v4
	v_mov_b32_e32 v40, v4
	v_mov_b32_e32 v41, v4
	v_mov_b32_e32 v42, v4
	v_mov_b32_e32 v43, v4
	v_mov_b32_e32 v48, v4
	v_mov_b32_e32 v49, v4
	v_mov_b32_e32 v50, v4
	v_mov_b32_e32 v51, v4
	v_mov_b32_e32 v56, v4
	v_mov_b32_e32 v57, v4
	v_mov_b32_e32 v58, v4
	v_mov_b32_e32 v59, v4
	v_mov_b32_e32 v12, v4
	v_mov_b32_e32 v13, v4
	v_mov_b32_e32 v14, v4
	v_mov_b32_e32 v15, v4
	v_mov_b32_e32 v20, v4
	v_mov_b32_e32 v21, v4
	v_mov_b32_e32 v22, v4
	v_mov_b32_e32 v23, v4
	v_mov_b32_e32 v28, v4
	v_mov_b32_e32 v29, v4
	v_mov_b32_e32 v30, v4
	v_mov_b32_e32 v31, v4
	v_mov_b32_e32 v36, v4
	v_mov_b32_e32 v37, v4
	v_mov_b32_e32 v38, v4
	v_mov_b32_e32 v39, v4
	v_mov_b32_e32 v44, v4
	v_mov_b32_e32 v45, v4
	v_mov_b32_e32 v46, v4
	v_mov_b32_e32 v47, v4
	v_mov_b32_e32 v52, v4
	v_mov_b32_e32 v53, v4
	v_mov_b32_e32 v54, v4
	v_mov_b32_e32 v55, v4
	v_mov_b32_e32 v60, v4
	v_mov_b32_e32 v61, v4
	v_mov_b32_e32 v62, v4
	v_mov_b32_e32 v63, v4
	v_mov_b32_e32 v64, v4
	v_mov_b32_e32 v65, v4
	v_mov_b32_e32 v66, v4
	v_mov_b32_e32 v67, v4
	v_mov_b32_e32 v68, v4
	v_mov_b32_e32 v69, v4
	v_mov_b32_e32 v70, v4
	v_mov_b32_e32 v71, v4
	v_mov_b32_e32 v72, v4
	v_mov_b32_e32 v73, v4
	v_mov_b32_e32 v74, v4
	v_mov_b32_e32 v75, v4
	v_mov_b32_e32 v84, v4
	v_mov_b32_e32 v85, v4
	v_mov_b32_e32 v86, v4
	v_mov_b32_e32 v87, v4
	v_mov_b32_e32 v88, v4
	v_mov_b32_e32 v89, v4
	v_mov_b32_e32 v90, v4
	v_mov_b32_e32 v91, v4
	v_mov_b32_e32 v116, v4
	v_mov_b32_e32 v117, v4
	v_mov_b32_e32 v118, v4
	v_mov_b32_e32 v119, v4
	v_mov_b32_e32 v120, v4
	v_mov_b32_e32 v121, v4
	v_mov_b32_e32 v122, v4
	v_mov_b32_e32 v123, v4
	v_mov_b32_e32 v132, v4
	v_mov_b32_e32 v133, v4
	v_mov_b32_e32 v134, v4
	v_mov_b32_e32 v135, v4
	v_mov_b32_e32 v136, v4
	v_mov_b32_e32 v137, v4
	v_mov_b32_e32 v138, v4
	v_mov_b32_e32 v139, v4
	v_mov_b32_e32 v76, v4
	v_mov_b32_e32 v77, v4
	v_mov_b32_e32 v78, v4
	v_mov_b32_e32 v79, v4
	v_mov_b32_e32 v80, v4
	v_mov_b32_e32 v81, v4
	v_mov_b32_e32 v82, v4
	v_mov_b32_e32 v83, v4
	v_mov_b32_e32 v92, v4
	v_mov_b32_e32 v93, v4
	v_mov_b32_e32 v94, v4
	v_mov_b32_e32 v95, v4
	v_mov_b32_e32 v96, v4
	v_mov_b32_e32 v97, v4
	v_mov_b32_e32 v98, v4
	v_mov_b32_e32 v99, v4
	v_mov_b32_e32 v124, v4
	v_mov_b32_e32 v125, v4
	v_mov_b32_e32 v126, v4
	v_mov_b32_e32 v127, v4
	v_mov_b32_e32 v128, v4
	v_mov_b32_e32 v129, v4
	v_mov_b32_e32 v130, v4
	v_mov_b32_e32 v131, v4
	v_mov_b32_e32 v140, v4
	v_mov_b32_e32 v141, v4
	v_mov_b32_e32 v142, v4
	v_mov_b32_e32 v143, v4
	v_mov_b32_e32 v144, v4
	v_mov_b32_e32 v145, v4
	v_mov_b32_e32 v146, v4
	v_mov_b32_e32 v147, v4
	s_cmp_eq_u32 s48, 1
	s_cbranch_scc1 .Ldn_unit_nobar
	s_cmp_eq_u64 s[0:1], 0
	s_cbranch_scc1 .Ldn_unit_nobar
	s_barrier
.Ldn_unit_nobar:
.LBB0_1817:
	s_add_u32 s4, s44, 0xfffc0080
	s_addc_u32 s5, s45, -1
	s_add_i32 s20, 0, 0x10000
	s_cmp_eq_u32 s57, 12
	s_cselect_b32 s25, s17, s5
	s_cselect_b32 s24, s36, s4
	s_cselect_b32 s5, s53, s56
	s_cselect_b32 s4, s54, s55
	s_add_i32 s33, 0, 0x14000
	v_add_u32_e32 v112, s20, v160
	v_add_u32_e32 v158, s33, v160
	ds_read_b128 v[100:103], v112
	ds_read_b128 v[104:107], v112 offset:1024
	ds_read_b128 v[108:111], v112 offset:2048
	ds_read_b128 v[112:115], v112 offset:3072
	ds_read_b128 v[170:173], v158
	ds_read_b128 v[174:177], v158 offset:1024
	ds_read_b128 v[178:181], v158 offset:2048
	ds_read_b128 v[182:185], v158 offset:3072
	v_lshl_add_u64 v[158:159], s[44:45], 0, v[154:155]
	s_add_i32 m0, s7, 0xc000
	ds_read_b128 v[186:189], v169
	ds_read_b128 v[190:193], v169 offset:1024
	ds_read_b128 v[194:197], v169 offset:2048
	ds_read_b128 v[198:201], v169 offset:3072
	ds_read_b128 v[202:205], v169 offset:4096
	ds_read_b128 v[208:211], v169 offset:5120
	ds_read_b128 v[224:227], v169 offset:6144
	ds_read_b128 v[228:231], v169 offset:7168
	global_load_lds_dwordx4 v[158:159], off
	v_lshl_add_u64 v[158:159], s[44:45], 0, v[156:157]
	s_add_i32 m0, s7, 0xe000
	s_nop 0
	global_load_lds_dwordx4 v[158:159], off
	s_waitcnt vmcnt(8)
	s_waitcnt lgkmcnt(0)
	s_barrier
; #define PG8_STAGE(bufoff, gbase, voff) do { _Pragma("unroll") for (int _i = 0; _i < 2; ++_i) \
;         __builtin_amdgcn_global_load_lds((const unsigned*)((const char*)(gbase) + (voff)[_i]), (PG8_LAS unsigned*)(lds + (bufoff) + ldsw + _i * 8192), 16, 0, 0); } while (0)
; #define PG8_STAGE_G(bufoff, kb, g) do { _Pragma("unroll") for (int _i = 0; _i < 2; ++_i) \
;         __builtin_amdgcn_global_load_lds((const unsigned*)(gA + (size_t)(kb) + (g)[_i]), (PG8_LAS unsigned*)(lds + (bufoff) + ldsw + _i * 8192), 16, 0, 0); } while (0)
; #define PG8_LDA(dst, b, h) do { _Pragma("unroll") for (int m = 0; m < 4; ++m) _Pragma("unroll") for (int k = 0; k < 2; ++k) dst[m][k] = *(const PG8_LAS bf16x8*)(lds + PG8_SA(b, h) + aoff + m * 2048 + k * 1024); } while (0)
; #define PG8_LDB(dst, b, h) do { _Pragma("unroll") for (int n = 0; n < 2; ++n) _Pragma("unroll") for (int k = 0; k < 2; ++k) dst[n][k] = *(const PG8_LAS bf16x8*)(lds + PG8_SB(b, h) + boff + n * 2048 + k * 1024); } while (0)
; #define PG8_WAIT_V(n) asm volatile("s_waitcnt vmcnt(" #n ")" ::: "memory")
; #define PG8_WAIT_L(n) asm volatile("s_waitcnt lgkmcnt(" #n ")" ::: "memory")
; #define PG8_BAR __builtin_amdgcn_s_barrier()
; #define PG8_SCHED __builtin_amdgcn_sched_barrier(0)
; template <class Epi, class Sched, bool ALIGN_EPI = false, bool SP2 = false, bool GATHER = false, bool HALFM = false>
; __device__ __forceinline__ void gemm_phase(PG8_LAS unsigned char* lds, const int Kdim, const Sched& S, const Epi& E) {
;     ...
;             PG8_WAIT_V(8); PG8_WAIT_L(0); PG8_BAR; PG8_MMA(0, 0, At, B0); PG8_MMA(0, 1, At, B1); PG8_BAR; PG8_SCHED;
;             if constexpr (!HALFM) PG8_LDA(At, 0, 1); PG8_STAGE(PG8_SB(0, 0), b2, voffB); PG8_STAGE(PG8_SB(0, 1), b2 + hstep, voffB); if constexpr (GATHER) PG8_STAGE_G(PG8_SA(0, 0), kb2, s0); else PG8_STAGE(PG8_SA(0, 0), a2, voffA);
;             PG8_WAIT_V(8); PG8_WAIT_L(0); PG8_BAR; if constexpr (!HALFM) { PG8_MMA(1, 0, At, B0); PG8_MMA(1, 1, At, B1); } PG8_BAR; PG8_SCHED;
;             PG8_LDB(B0, 1, 0); PG8_LDB(B1, 1, 1); PG8_SCHED; PG8_LDA(At, 1, 0); if constexpr (GATHER) PG8_STAGE_G(PG8_SA(0, 1), kb2, s1); else PG8_STAGE(PG8_SA(0, 1), a2 + hstep, voffA);
;             PG8_WAIT_V(8); PG8_WAIT_L(0); PG8_BAR; PG8_MMA(0, 0, At, B0); PG8_MMA(0, 1, At, B1); PG8_BAR; PG8_SCHED;
	s_setprio 1
	s_waitcnt lgkmcnt(0)
	v_mfma_f32_16x16x32_bf16 v[144:147], v[100:103], v[186:189], v[144:147]
	v_mfma_f32_16x16x32_bf16 v[140:143], v[108:111], v[186:189], v[140:143]
	v_mfma_f32_16x16x32_bf16 v[128:131], v[100:103], v[194:197], v[128:131]
	v_mfma_f32_16x16x32_bf16 v[124:127], v[108:111], v[194:197], v[124:127]
	v_mfma_f32_16x16x32_bf16 v[96:99], v[100:103], v[202:205], v[96:99]
	v_mfma_f32_16x16x32_bf16 v[92:95], v[108:111], v[202:205], v[92:95]
	v_mfma_f32_16x16x32_bf16 v[80:83], v[100:103], v[224:227], v[80:83]
	v_mfma_f32_16x16x32_bf16 v[76:79], v[108:111], v[224:227], v[76:79]
	v_mfma_f32_16x16x32_bf16 v[144:147], v[104:107], v[190:193], v[144:147]
	v_mfma_f32_16x16x32_bf16 v[140:143], v[112:115], v[190:193], v[140:143]
	v_mfma_f32_16x16x32_bf16 v[128:131], v[104:107], v[198:201], v[128:131]
	v_mfma_f32_16x16x32_bf16 v[124:127], v[112:115], v[198:201], v[124:127]
	v_mfma_f32_16x16x32_bf16 v[96:99], v[104:107], v[208:211], v[96:99]
	v_mfma_f32_16x16x32_bf16 v[92:95], v[112:115], v[208:211], v[92:95]
	v_mfma_f32_16x16x32_bf16 v[80:83], v[104:107], v[228:231], v[80:83]
	v_mfma_f32_16x16x32_bf16 v[76:79], v[112:115], v[228:231], v[76:79]
	s_setprio 0
	s_setprio 1
	v_mfma_f32_16x16x32_bf16 v[136:139], v[170:173], v[186:189], v[136:139]
	v_mfma_f32_16x16x32_bf16 v[132:135], v[178:181], v[186:189], v[132:135]
	v_mfma_f32_16x16x32_bf16 v[120:123], v[170:173], v[194:197], v[120:123]
	v_mfma_f32_16x16x32_bf16 v[116:119], v[178:181], v[194:197], v[116:119]
	v_mfma_f32_16x16x32_bf16 v[88:91], v[170:173], v[202:205], v[88:91]
	v_mfma_f32_16x16x32_bf16 v[84:87], v[178:181], v[202:205], v[84:87]
	v_mfma_f32_16x16x32_bf16 v[72:75], v[170:173], v[224:227], v[72:75]
	v_mfma_f32_16x16x32_bf16 v[68:71], v[178:181], v[224:227], v[68:71]
	v_mfma_f32_16x16x32_bf16 v[136:139], v[174:177], v[190:193], v[136:139]
	v_mfma_f32_16x16x32_bf16 v[132:135], v[182:185], v[190:193], v[132:135]
	v_mfma_f32_16x16x32_bf16 v[120:123], v[174:177], v[198:201], v[120:123]
	v_mfma_f32_16x16x32_bf16 v[116:119], v[182:185], v[198:201], v[116:119]
	v_mfma_f32_16x16x32_bf16 v[88:91], v[174:177], v[208:211], v[88:91]
	v_mfma_f32_16x16x32_bf16 v[84:87], v[182:185], v[208:211], v[84:87]
	v_mfma_f32_16x16x32_bf16 v[72:75], v[174:177], v[228:231], v[72:75]
	v_mfma_f32_16x16x32_bf16 v[68:71], v[182:185], v[228:231], v[68:71]
	s_setprio 0
	s_barrier
	s_add_i32 s20, s20, s13
	v_lshl_add_u64 v[158:159], s[4:5], 0, v[2:3]
	s_mov_b32 m0, s20
	ds_read_b128 v[186:189], v169 offset:16384
	ds_read_b128 v[190:193], v169 offset:17408
	ds_read_b128 v[194:197], v169 offset:18432
	ds_read_b128 v[198:201], v169 offset:19456
	ds_read_b128 v[202:205], v169 offset:20480
	ds_read_b128 v[208:211], v169 offset:21504
	ds_read_b128 v[224:227], v169 offset:22528
	ds_read_b128 v[228:231], v169 offset:23552
	global_load_lds_dwordx4 v[158:159], off
	s_add_i32 m0, s20, 0x2000
	s_add_u32 s20, s4, 0x40000
	v_lshl_add_u64 v[216:217], s[4:5], 0, v[148:149]
	s_addc_u32 s21, s5, 0
	s_add_i32 s33, s33, s13
	global_load_lds_dwordx4 v[216:217], off
	v_lshl_add_u64 v[218:219], s[20:21], 0, v[2:3]
	s_mov_b32 m0, s33
	v_lshl_add_u64 v[220:221], s[24:25], 0, v[150:151]
	global_load_lds_dwordx4 v[218:219], off
	v_lshl_add_u64 v[218:219], s[20:21], 0, v[148:149]
	s_add_i32 m0, s33, 0x2000
	s_nop 0
	global_load_lds_dwordx4 v[218:219], off
	v_lshl_add_u64 v[218:219], s[24:25], 0, v[152:153]
	s_mov_b32 m0, s7
	s_nop 0
	global_load_lds_dwordx4 v[218:219], off
	s_mov_b32 m0, s22
	s_nop 0
	global_load_lds_dwordx4 v[220:221], off
	s_waitcnt vmcnt(8)
	s_waitcnt lgkmcnt(0)
	s_barrier
	s_setprio 1
	s_waitcnt lgkmcnt(0)
	v_mfma_f32_16x16x32_bf16 v[64:67], v[100:103], v[186:189], v[64:67]
	v_mfma_f32_16x16x32_bf16 v[60:63], v[108:111], v[186:189], v[60:63]
	v_mfma_f32_16x16x32_bf16 v[52:55], v[100:103], v[194:197], v[52:55]
	v_mfma_f32_16x16x32_bf16 v[44:47], v[108:111], v[194:197], v[44:47]
	v_mfma_f32_16x16x32_bf16 v[36:39], v[100:103], v[202:205], v[36:39]
	v_mfma_f32_16x16x32_bf16 v[28:31], v[108:111], v[202:205], v[28:31]
	v_mfma_f32_16x16x32_bf16 v[20:23], v[100:103], v[224:227], v[20:23]
	v_mfma_f32_16x16x32_bf16 v[12:15], v[108:111], v[224:227], v[12:15]
	v_mfma_f32_16x16x32_bf16 v[64:67], v[104:107], v[190:193], v[64:67]
	v_mfma_f32_16x16x32_bf16 v[60:63], v[112:115], v[190:193], v[60:63]
	v_mfma_f32_16x16x32_bf16 v[52:55], v[104:107], v[198:201], v[52:55]
	v_mfma_f32_16x16x32_bf16 v[44:47], v[112:115], v[198:201], v[44:47]
	v_mfma_f32_16x16x32_bf16 v[36:39], v[104:107], v[208:211], v[36:39]
	v_mfma_f32_16x16x32_bf16 v[28:31], v[112:115], v[208:211], v[28:31]
	v_mfma_f32_16x16x32_bf16 v[20:23], v[104:107], v[228:231], v[20:23]
	v_mfma_f32_16x16x32_bf16 v[12:15], v[112:115], v[228:231], v[12:15]
	s_setprio 0
	s_setprio 1
	v_mfma_f32_16x16x32_bf16 v[56:59], v[170:173], v[186:189], v[56:59]
	v_mfma_f32_16x16x32_bf16 v[48:51], v[178:181], v[186:189], v[48:51]
	v_mfma_f32_16x16x32_bf16 v[40:43], v[170:173], v[194:197], v[40:43]
	v_mfma_f32_16x16x32_bf16 v[32:35], v[178:181], v[194:197], v[32:35]
	v_mfma_f32_16x16x32_bf16 v[24:27], v[170:173], v[202:205], v[24:27]
	v_mfma_f32_16x16x32_bf16 v[16:19], v[178:181], v[202:205], v[16:19]
	v_mfma_f32_16x16x32_bf16 v[8:11], v[170:173], v[224:227], v[8:11]
	v_mfma_f32_16x16x32_bf16 v[4:7], v[178:181], v[224:227], v[4:7]
	v_mfma_f32_16x16x32_bf16 v[56:59], v[174:177], v[190:193], v[56:59]
	v_mfma_f32_16x16x32_bf16 v[48:51], v[182:185], v[190:193], v[48:51]
	v_mfma_f32_16x16x32_bf16 v[40:43], v[174:177], v[198:201], v[40:43]
	v_mfma_f32_16x16x32_bf16 v[32:35], v[182:185], v[198:201], v[32:35]
	v_mfma_f32_16x16x32_bf16 v[24:27], v[174:177], v[208:211], v[24:27]
	v_mfma_f32_16x16x32_bf16 v[16:19], v[182:185], v[208:211], v[16:19]
	v_mfma_f32_16x16x32_bf16 v[8:11], v[174:177], v[228:231], v[8:11]
	v_mfma_f32_16x16x32_bf16 v[4:7], v[182:185], v[228:231], v[4:7]
	s_setprio 0
	s_barrier
; #define PG8_STAGE(bufoff, gbase, voff) do { _Pragma("unroll") for (int _i = 0; _i < 2; ++_i) \
;         __builtin_amdgcn_global_load_lds((const unsigned*)((const char*)(gbase) + (voff)[_i]), (PG8_LAS unsigned*)(lds + (bufoff) + ldsw + _i * 8192), 16, 0, 0); } while (0)
; #define PG8_STAGE_G(bufoff, kb, g) do { _Pragma("unroll") for (int _i = 0; _i < 2; ++_i) \
;         __builtin_amdgcn_global_load_lds((const unsigned*)(gA + (size_t)(kb) + (g)[_i]), (PG8_LAS unsigned*)(lds + (bufoff) + ldsw + _i * 8192), 16, 0, 0); } while (0)
; #define PG8_LDA(dst, b, h) do { _Pragma("unroll") for (int m = 0; m < 4; ++m) _Pragma("unroll") for (int k = 0; k < 2; ++k) dst[m][k] = *(const PG8_LAS bf16x8*)(lds + PG8_SA(b, h) + aoff + m * 2048 + k * 1024); } while (0)
; #define PG8_LDB(dst, b, h) do { _Pragma("unroll") for (int n = 0; n < 2; ++n) _Pragma("unroll") for (int k = 0; k < 2; ++k) dst[n][k] = *(const PG8_LAS bf16x8*)(lds + PG8_SB(b, h) + boff + n * 2048 + k * 1024); } while (0)
; #define PG8_MMA(ai, bj, At, Bt) do { __builtin_amdgcn_s_setprio(1); _Pragma("unroll") for (int m = 0; m < 4; ++m) _Pragma("unroll") for (int n = 0; n < 2; ++n) _Pragma("unroll") for (int k = 0; k < 2; ++k) \
;         acc[ai][bj][m][n] = __builtin_amdgcn_mfma_f32_16x16x32_bf16(Bt[n][k], At[m][k], acc[ai][bj][m][n], 0, 0, 0); __builtin_amdgcn_s_setprio(0); } while (0)
; #define PG8_WAIT_V(n) asm volatile("s_waitcnt vmcnt(" #n ")" ::: "memory")
; #define PG8_WAIT_L(n) asm volatile("s_waitcnt lgkmcnt(" #n ")" ::: "memory")
; #define PG8_BAR __builtin_amdgcn_s_barrier()
; template <class Epi, class Sched, bool ALIGN_EPI = false, bool SP2 = false, bool GATHER = false, bool HALFM = false>
; __device__ __forceinline__ void gemm_phase(PG8_LAS unsigned char* lds, const int Kdim, const Sched& S, const Epi& E) {
;     ...
;             PG8_LDB(B0, 1, 0); PG8_LDB(B1, 1, 1); PG8_SCHED; PG8_LDA(At, 1, 0); if constexpr (GATHER) PG8_STAGE_G(PG8_SA(0, 1), kb2, s1); else PG8_STAGE(PG8_SA(0, 1), a2 + hstep, voffA);
;             PG8_WAIT_V(8); PG8_WAIT_L(0); PG8_BAR; PG8_MMA(0, 0, At, B0); PG8_MMA(0, 1, At, B1); PG8_BAR; PG8_SCHED;
;             if constexpr (!HALFM) PG8_LDA(At, 1, 1); PG8_STAGE(PG8_SB(1, 0), b3, voffB); PG8_STAGE(PG8_SB(1, 1), b3 + hstep, voffB); if constexpr (GATHER) PG8_STAGE_G(PG8_SA(1, 0), kb2 + kstep, s0); else PG8_STAGE(PG8_SA(1, 0), a3, voffA);
	s_add_i32 s33, 0, 0x18000
	s_add_i32 s76, 0, 0x1c000
	v_add_u32_e32 v112, s33, v160
	v_add_u32_e32 v182, s76, v160
	ds_read_b128 v[100:103], v112
	ds_read_b128 v[104:107], v112 offset:1024
	ds_read_b128 v[108:111], v112 offset:2048
	ds_read_b128 v[112:115], v112 offset:3072
	ds_read_b128 v[170:173], v182
	ds_read_b128 v[174:177], v182 offset:1024
	ds_read_b128 v[178:181], v182 offset:2048
	ds_read_b128 v[182:185], v182 offset:3072
	s_add_u32 s20, s24, 0x40000
	s_addc_u32 s21, s25, 0
	s_mov_b32 m0, s23
	v_lshl_add_u64 v[232:233], s[20:21], 0, v[152:153]
	ds_read_b128 v[186:189], v169 offset:32768
	ds_read_b128 v[190:193], v169 offset:33792
	ds_read_b128 v[194:197], v169 offset:34816
	ds_read_b128 v[198:201], v169 offset:35840
	ds_read_b128 v[202:205], v169 offset:36864
	ds_read_b128 v[208:211], v169 offset:37888
	ds_read_b128 v[224:227], v169 offset:38912
	ds_read_b128 v[228:231], v169 offset:39936
	global_load_lds_dwordx4 v[232:233], off
	v_lshl_add_u64 v[232:233], s[20:21], 0, v[150:151]
	s_mov_b32 m0, s26
	s_nop 0
	global_load_lds_dwordx4 v[232:233], off
	s_waitcnt vmcnt(8)
	s_waitcnt lgkmcnt(0)
	s_barrier
	s_setprio 1
	s_waitcnt lgkmcnt(0)
	v_mfma_f32_16x16x32_bf16 v[144:147], v[100:103], v[186:189], v[144:147]
	v_mfma_f32_16x16x32_bf16 v[140:143], v[108:111], v[186:189], v[140:143]
	v_mfma_f32_16x16x32_bf16 v[128:131], v[100:103], v[194:197], v[128:131]
	v_mfma_f32_16x16x32_bf16 v[124:127], v[108:111], v[194:197], v[124:127]
	v_mfma_f32_16x16x32_bf16 v[96:99], v[100:103], v[202:205], v[96:99]
	v_mfma_f32_16x16x32_bf16 v[92:95], v[108:111], v[202:205], v[92:95]
	v_mfma_f32_16x16x32_bf16 v[80:83], v[100:103], v[224:227], v[80:83]
	v_mfma_f32_16x16x32_bf16 v[76:79], v[108:111], v[224:227], v[76:79]
	v_mfma_f32_16x16x32_bf16 v[144:147], v[104:107], v[190:193], v[144:147]
	v_mfma_f32_16x16x32_bf16 v[140:143], v[112:115], v[190:193], v[140:143]
	v_mfma_f32_16x16x32_bf16 v[128:131], v[104:107], v[198:201], v[128:131]
	v_mfma_f32_16x16x32_bf16 v[124:127], v[112:115], v[198:201], v[124:127]
	v_mfma_f32_16x16x32_bf16 v[96:99], v[104:107], v[208:211], v[96:99]
	v_mfma_f32_16x16x32_bf16 v[92:95], v[112:115], v[208:211], v[92:95]
	v_mfma_f32_16x16x32_bf16 v[80:83], v[104:107], v[228:231], v[80:83]
	v_mfma_f32_16x16x32_bf16 v[76:79], v[112:115], v[228:231], v[76:79]
	s_setprio 0
	s_setprio 1
	v_mfma_f32_16x16x32_bf16 v[136:139], v[170:173], v[186:189], v[136:139]
	v_mfma_f32_16x16x32_bf16 v[132:135], v[178:181], v[186:189], v[132:135]
	v_mfma_f32_16x16x32_bf16 v[120:123], v[170:173], v[194:197], v[120:123]
	v_mfma_f32_16x16x32_bf16 v[116:119], v[178:181], v[194:197], v[116:119]
	v_mfma_f32_16x16x32_bf16 v[88:91], v[170:173], v[202:205], v[88:91]
	v_mfma_f32_16x16x32_bf16 v[84:87], v[178:181], v[202:205], v[84:87]
	v_mfma_f32_16x16x32_bf16 v[72:75], v[170:173], v[224:227], v[72:75]
	v_mfma_f32_16x16x32_bf16 v[68:71], v[178:181], v[224:227], v[68:71]
	v_mfma_f32_16x16x32_bf16 v[136:139], v[174:177], v[190:193], v[136:139]
	v_mfma_f32_16x16x32_bf16 v[132:135], v[182:185], v[190:193], v[132:135]
	v_mfma_f32_16x16x32_bf16 v[120:123], v[174:177], v[198:201], v[120:123]
	v_mfma_f32_16x16x32_bf16 v[116:119], v[182:185], v[198:201], v[116:119]
	v_mfma_f32_16x16x32_bf16 v[88:91], v[174:177], v[208:211], v[88:91]
	v_mfma_f32_16x16x32_bf16 v[84:87], v[182:185], v[208:211], v[84:87]
	v_mfma_f32_16x16x32_bf16 v[72:75], v[174:177], v[228:231], v[72:75]
	v_mfma_f32_16x16x32_bf16 v[68:71], v[182:185], v[228:231], v[68:71]
	s_setprio 0
	s_barrier
	s_add_i32 s20, s33, s13
	v_lshl_add_u64 v[158:159], v[158:159], 0, s[34:35]
	s_mov_b32 m0, s20
	ds_read_b128 v[186:189], v169 offset:49152
	ds_read_b128 v[190:193], v169 offset:50176
	ds_read_b128 v[194:197], v169 offset:51200
	ds_read_b128 v[198:201], v169 offset:52224
	ds_read_b128 v[202:205], v169 offset:53248
	ds_read_b128 v[208:211], v169 offset:54272
	ds_read_b128 v[224:227], v169 offset:55296
	ds_read_b128 v[228:231], v169 offset:56320
	global_load_lds_dwordx4 v[158:159], off
	s_add_i32 m0, s20, 0x2000
	s_add_u32 s4, s4, 0x40080
	v_lshl_add_u64 v[158:159], v[216:217], 0, s[34:35]
	s_addc_u32 s5, s5, 0
	s_add_i32 s20, s76, s13
	global_load_lds_dwordx4 v[158:159], off
	v_lshl_add_u64 v[158:159], s[4:5], 0, v[2:3]
	s_mov_b32 m0, s20
	s_nop 0
	global_load_lds_dwordx4 v[158:159], off
	v_lshl_add_u64 v[158:159], s[4:5], 0, v[148:149]
	s_add_i32 m0, s20, 0x2000
	s_nop 0
	global_load_lds_dwordx4 v[158:159], off
	v_lshl_add_u64 v[158:159], v[218:219], 0, s[34:35]
	s_mov_b32 m0, s46
	s_nop 0
	global_load_lds_dwordx4 v[158:159], off
	v_lshl_add_u64 v[158:159], v[220:221], 0, s[34:35]
	s_mov_b32 m0, s47
	s_nop 0
	global_load_lds_dwordx4 v[158:159], off
	s_waitcnt vmcnt(8)
	s_waitcnt lgkmcnt(0)
	s_barrier
; __device__ __forceinline__ unsigned cvt_pk_bf16(float lo, float hi) { unsigned r; asm volatile("v_cvt_pk_bf16_f32 %0, %1, %2" : "=v"(r) : "v"(lo), "v"(hi)); return r; }
; #define PG8_STAGE(bufoff, gbase, voff) do { _Pragma("unroll") for (int _i = 0; _i < 2; ++_i) \
;         __builtin_amdgcn_global_load_lds((const unsigned*)((const char*)(gbase) + (voff)[_i]), (PG8_LAS unsigned*)(lds + (bufoff) + ldsw + _i * 8192), 16, 0, 0); } while (0)
; #define PG8_WAIT_V(n) asm volatile("s_waitcnt vmcnt(" #n ")" ::: "memory")
; #define PG8_BAR __builtin_amdgcn_s_barrier()
; template <class Epi, class Sched, bool ALIGN_EPI = false, bool SP2 = false, bool GATHER = false, bool HALFM = false>
; __device__ __forceinline__ void gemm_phase(PG8_LAS unsigned char* lds, const int Kdim, const Sched& S, const Epi& E) {
;     ...
;             PG8_WAIT_V(8); PG8_WAIT_L(0); PG8_BAR; PG8_MMA(0, 0, At, B0); PG8_MMA(0, 1, At, B1); PG8_BAR; PG8_SCHED;
;             if constexpr (!HALFM) PG8_LDA(At, 1, 1); PG8_STAGE(PG8_SB(1, 0), b3, voffB); PG8_STAGE(PG8_SB(1, 1), b3 + hstep, voffB); if constexpr (GATHER) PG8_STAGE_G(PG8_SA(1, 0), kb2 + kstep, s0); else PG8_STAGE(PG8_SA(1, 0), a3, voffA);
;             PG8_WAIT_V(8); PG8_WAIT_L(0); PG8_BAR; if constexpr (!HALFM) { PG8_MMA(1, 0, At, B0); PG8_MMA(1, 1, At, B1); } PG8_BAR; PG8_SCHED;
;     __device__ __forceinline__ void operator()(const pg8::f32x4 (&acc)[2][2][4][2], const pg8::Unit& u, int wr, int wc, int fr, int fq) const {
;     ...
;         const int col0 = u.pn * 256 + wc * 32 + 8 * fq;
;         f32x4 bv[2][2];
; #pragma unroll
;         for (int bj = 0; bj < 2; ++bj)
; #pragma unroll
;             for (int n = 0; n < 2; ++n) bv[bj][n] = *(const f32x4*)(b_down + u.e * 1024 + col0 + bj * 128 + 4 * n);
; #pragma unroll
;         for (int ai = 0; ai < 2; ++ai)
; #pragma unroll
;             for (int m = 0; m < 4; ++m) {
;                 bf16_t* rowp = YS + (size_t)(u.pm + ai * 128 + wr * 64 + m * 16 + fr) * 1024 + col0;
; #pragma unroll
;                 for (int bj = 0; bj < 2; ++bj) {
;                     const f32x4 v0 = acc[ai][bj][m][0] + bv[bj][0], v1 = acc[ai][bj][m][1] + bv[bj][1];
;                     pg8::u32x4 w; w.x = pg8::cvt_pk_bf16(v0[0], v0[1]); w.y = pg8::cvt_pk_bf16(v0[2], v0[3]); w.z = pg8::cvt_pk_bf16(v1[0], v1[1]); w.w = pg8::cvt_pk_bf16(v1[2], v1[3]);
;                     *(pg8::u32x4*)(rowp + bj * 128) = w;
	s_setprio 1
	s_waitcnt lgkmcnt(0)
	v_mfma_f32_16x16x32_bf16 v[64:67], v[100:103], v[186:189], v[64:67]
	v_mfma_f32_16x16x32_bf16 v[60:63], v[108:111], v[186:189], v[60:63]
	v_mfma_f32_16x16x32_bf16 v[52:55], v[100:103], v[194:197], v[52:55]
	v_mfma_f32_16x16x32_bf16 v[44:47], v[108:111], v[194:197], v[44:47]
	v_mfma_f32_16x16x32_bf16 v[36:39], v[100:103], v[202:205], v[36:39]
	v_mfma_f32_16x16x32_bf16 v[28:31], v[108:111], v[202:205], v[28:31]
	v_mfma_f32_16x16x32_bf16 v[20:23], v[100:103], v[224:227], v[20:23]
	v_mfma_f32_16x16x32_bf16 v[12:15], v[108:111], v[224:227], v[12:15]
	v_mfma_f32_16x16x32_bf16 v[64:67], v[104:107], v[190:193], v[64:67]
	v_mfma_f32_16x16x32_bf16 v[60:63], v[112:115], v[190:193], v[60:63]
	v_mfma_f32_16x16x32_bf16 v[52:55], v[104:107], v[198:201], v[52:55]
	v_mfma_f32_16x16x32_bf16 v[44:47], v[112:115], v[198:201], v[44:47]
	v_mfma_f32_16x16x32_bf16 v[36:39], v[104:107], v[208:211], v[36:39]
	v_mfma_f32_16x16x32_bf16 v[28:31], v[112:115], v[208:211], v[28:31]
	v_mfma_f32_16x16x32_bf16 v[20:23], v[104:107], v[228:231], v[20:23]
	v_mfma_f32_16x16x32_bf16 v[12:15], v[112:115], v[228:231], v[12:15]
	s_setprio 0
	s_setprio 1
	v_mfma_f32_16x16x32_bf16 v[56:59], v[170:173], v[186:189], v[56:59]
	v_mfma_f32_16x16x32_bf16 v[48:51], v[178:181], v[186:189], v[48:51]
	v_mfma_f32_16x16x32_bf16 v[40:43], v[170:173], v[194:197], v[40:43]
	v_mfma_f32_16x16x32_bf16 v[32:35], v[178:181], v[194:197], v[32:35]
	v_mfma_f32_16x16x32_bf16 v[24:27], v[170:173], v[202:205], v[24:27]
	v_mfma_f32_16x16x32_bf16 v[16:19], v[178:181], v[202:205], v[16:19]
	v_mfma_f32_16x16x32_bf16 v[8:11], v[170:173], v[224:227], v[8:11]
	v_mfma_f32_16x16x32_bf16 v[4:7], v[178:181], v[224:227], v[4:7]
	v_mfma_f32_16x16x32_bf16 v[56:59], v[174:177], v[190:193], v[56:59]
	v_mfma_f32_16x16x32_bf16 v[48:51], v[182:185], v[190:193], v[48:51]
	v_mfma_f32_16x16x32_bf16 v[40:43], v[174:177], v[198:201], v[40:43]
	v_mfma_f32_16x16x32_bf16 v[32:35], v[182:185], v[198:201], v[32:35]
	v_mfma_f32_16x16x32_bf16 v[24:27], v[174:177], v[208:211], v[24:27]
	v_mfma_f32_16x16x32_bf16 v[16:19], v[182:185], v[208:211], v[16:19]
	v_mfma_f32_16x16x32_bf16 v[8:11], v[174:177], v[228:231], v[8:11]
	v_mfma_f32_16x16x32_bf16 v[4:7], v[182:185], v[228:231], v[4:7]
	s_setprio 0
	s_barrier
	s_add_i32 s57, s57, 2
	s_add_u32 s44, s44, 0x100
	s_addc_u32 s45, s45, 0
	s_add_u32 s55, s55, 0x100
	s_addc_u32 s56, s56, 0
	s_cmp_gt_u32 s57, 13
	s_cbranch_scc0 .LBB0_1817
	s_and_b64 vcc, exec, s[14:15]
	s_cbranch_vccz .LBB0_1820
	s_barrier
.LBB0_1820:
	s_lshl_b32 s4, s51, 10
	s_ashr_i32 s5, s4, 31
	s_lshl_b64 s[4:5], s[4:5], 2
	v_lshl_or_b32 v158, s52, 8, v161
	s_add_u32 s4, s27, s4
	s_addc_u32 s5, s37, s5
	v_ashrrev_i32_e32 v159, 31, v158
	v_lshl_add_u64 v[104:105], v[158:159], 2, s[4:5]
	global_load_dwordx4 v[108:111], v[104:105], off offset:16
	global_load_dwordx4 v[112:115], v[104:105], off
	global_load_dwordx4 v[100:103], v[104:105], off offset:528
	s_nop 0
	global_load_dwordx4 v[104:107], v[104:105], off offset:512
	v_add_u32_e32 v170, s6, v1
	v_ashrrev_i32_e32 v171, 31, v170
	v_lshlrev_b64 v[170:171], 11, v[170:171]
	v_lshl_add_u64 v[170:171], s[10:11], 0, v[170:171]
	v_lshlrev_b64 v[158:159], 1, v[158:159]
	v_lshl_add_u64 v[170:171], v[170:171], 0, v[158:159]
	v_readlane_b32 s76, v255, 5
	s_mov_b64 s[4:5], -1
	s_andn2_b64 vcc, exec, s[42:43]
	v_readlane_b32 s77, v255, 6
	s_movk_i32 s33, 0x1dff
	s_waitcnt vmcnt(0)
	v_pk_add_f32 v[172:173], v[142:143], v[110:111]
	v_pk_add_f32 v[146:147], v[146:147], v[114:115]
	v_pk_add_f32 v[144:145], v[144:145], v[112:113]
	v_pk_add_f32 v[142:143], v[140:141], v[108:109]
	v_cvt_pk_bf16_f32 v140, v144, v145
	v_cvt_pk_bf16_f32 v141, v146, v147
	v_pk_add_f32 v[136:137], v[136:137], v[104:105]
	v_cvt_pk_bf16_f32 v142, v142, v143
	v_cvt_pk_bf16_f32 v143, v172, v173
	global_store_dwordx4 v[170:171], v[140:143], off
	v_pk_add_f32 v[138:139], v[138:139], v[106:107]
	v_pk_add_f32 v[130:131], v[130:131], v[114:115]
	v_pk_add_f32 v[140:141], v[134:135], v[102:103]
	v_pk_add_f32 v[134:135], v[132:133], v[100:101]
	v_cvt_pk_bf16_f32 v132, v136, v137
	v_cvt_pk_bf16_f32 v133, v138, v139
	v_pk_add_f32 v[128:129], v[128:129], v[112:113]
	v_cvt_pk_bf16_f32 v134, v134, v135
	v_cvt_pk_bf16_f32 v135, v140, v141
	global_store_dwordx4 v[170:171], v[132:135], off offset:256
	v_pk_add_f32 v[120:121], v[120:121], v[104:105]
	v_pk_add_f32 v[122:123], v[122:123], v[106:107]
	v_add_u32_e32 v132, s6, v162
	v_ashrrev_i32_e32 v133, 31, v132
	v_lshlrev_b64 v[132:133], 11, v[132:133]
	v_lshl_add_u64 v[132:133], s[10:11], 0, v[132:133]
	v_lshl_add_u64 v[132:133], v[132:133], 0, v[158:159]
	v_pk_add_f32 v[134:135], v[126:127], v[110:111]
	v_pk_add_f32 v[126:127], v[124:125], v[108:109]
	v_cvt_pk_bf16_f32 v124, v128, v129
	v_cvt_pk_bf16_f32 v125, v130, v131
	v_pk_add_f32 v[98:99], v[98:99], v[114:115]
	v_cvt_pk_bf16_f32 v126, v126, v127
	v_cvt_pk_bf16_f32 v127, v134, v135
	global_store_dwordx4 v[132:133], v[124:127], off
	v_pk_add_f32 v[96:97], v[96:97], v[112:113]
	v_pk_add_f32 v[88:89], v[88:89], v[104:105]
	v_pk_add_f32 v[124:125], v[118:119], v[102:103]
	v_pk_add_f32 v[118:119], v[116:117], v[100:101]
	v_cvt_pk_bf16_f32 v116, v120, v121
	v_cvt_pk_bf16_f32 v117, v122, v123
	v_pk_add_f32 v[90:91], v[90:91], v[106:107]
	v_cvt_pk_bf16_f32 v118, v118, v119
	v_cvt_pk_bf16_f32 v119, v124, v125
	global_store_dwordx4 v[132:133], v[116:119], off offset:256
	v_pk_add_f32 v[82:83], v[82:83], v[114:115]
	v_pk_add_f32 v[80:81], v[80:81], v[112:113]
; __device__ __forceinline__ unsigned cvt_pk_bf16(float lo, float hi) { unsigned r; asm volatile("v_cvt_pk_bf16_f32 %0, %1, %2" : "=v"(r) : "v"(lo), "v"(hi)); return r; }
; #define PG8_BAR __builtin_amdgcn_s_barrier()
; template <class Epi, class Sched, bool ALIGN_EPI = false, bool SP2 = false, bool GATHER = false, bool HALFM = false>
; __device__ __forceinline__ void gemm_phase(PG8_LAS unsigned char* lds, const int Kdim, const Sched& S, const Epi& E) {
;     ...
;         if (!has_next) break;
; #pragma unroll
;         for (int a = 0; a < 2; ++a)
; #pragma unroll
;             for (int b = 0; b < 2; ++b)
; #pragma unroll
;                 for (int m = 0; m < 4; ++m)
; #pragma unroll
;                     for (int n = 0; n < 2; ++n) acc[a][b][m][n] = (f32x4){0.f, 0.f, 0.f, 0.f};
;         cur = nxt; cA = nA; cB = nB; ++ui;
;         if constexpr (GATHER) {
; #pragma unroll
;             for (int h = 0; h < 2; ++h)
; #pragma unroll
;                 for (int i = 0; i < 2; ++i) { gc[h][i] = gn[h][i]; if (has_nn) gn[h][i] = (unsigned)ix[h][i] * (unsigned)(K * 2) + CA2[i]; } }
;         if constexpr (ALIGN_EPI) { if (wr == 1) PG8_BAR; }
;     __device__ __forceinline__ void operator()(const pg8::f32x4 (&acc)[2][2][4][2], const pg8::Unit& u, int wr, int wc, int fr, int fq) const {
;     ...
;         for (int ai = 0; ai < 2; ++ai)
; #pragma unroll
;             for (int m = 0; m < 4; ++m) {
;                 bf16_t* rowp = YS + (size_t)(u.pm + ai * 128 + wr * 64 + m * 16 + fr) * 1024 + col0;
; #pragma unroll
;                 for (int bj = 0; bj < 2; ++bj) {
;                     const f32x4 v0 = acc[ai][bj][m][0] + bv[bj][0], v1 = acc[ai][bj][m][1] + bv[bj][1];
;                     pg8::u32x4 w; w.x = pg8::cvt_pk_bf16(v0[0], v0[1]); w.y = pg8::cvt_pk_bf16(v0[2], v0[3]); w.z = pg8::cvt_pk_bf16(v1[0], v1[1]); w.w = pg8::cvt_pk_bf16(v1[2], v1[3]);
;                     *(pg8::u32x4*)(rowp + bj * 128) = w;
	v_add_u32_e32 v116, s6, v163
	v_ashrrev_i32_e32 v117, 31, v116
	v_lshlrev_b64 v[116:117], 11, v[116:117]
	v_lshl_add_u64 v[116:117], s[10:11], 0, v[116:117]
	v_lshl_add_u64 v[116:117], v[116:117], 0, v[158:159]
	v_pk_add_f32 v[118:119], v[94:95], v[110:111]
	v_pk_add_f32 v[94:95], v[92:93], v[108:109]
	v_cvt_pk_bf16_f32 v92, v96, v97
	v_cvt_pk_bf16_f32 v93, v98, v99
	v_pk_add_f32 v[72:73], v[72:73], v[104:105]
	v_cvt_pk_bf16_f32 v94, v94, v95
	v_cvt_pk_bf16_f32 v95, v118, v119
	global_store_dwordx4 v[116:117], v[92:95], off
	v_pk_add_f32 v[74:75], v[74:75], v[106:107]
	v_pk_add_f32 v[66:67], v[66:67], v[114:115]
	v_pk_add_f32 v[92:93], v[86:87], v[102:103]
	v_pk_add_f32 v[86:87], v[84:85], v[100:101]
	v_cvt_pk_bf16_f32 v84, v88, v89
	v_cvt_pk_bf16_f32 v85, v90, v91
	v_pk_add_f32 v[64:65], v[64:65], v[112:113]
	v_cvt_pk_bf16_f32 v86, v86, v87
	v_cvt_pk_bf16_f32 v87, v92, v93
	global_store_dwordx4 v[116:117], v[84:87], off offset:256
	v_pk_add_f32 v[56:57], v[56:57], v[104:105]
	v_pk_add_f32 v[58:59], v[58:59], v[106:107]
	v_add_u32_e32 v84, s6, v164
	v_ashrrev_i32_e32 v85, 31, v84
	v_lshlrev_b64 v[84:85], 11, v[84:85]
	v_lshl_add_u64 v[84:85], s[10:11], 0, v[84:85]
	v_lshl_add_u64 v[84:85], v[84:85], 0, v[158:159]
	v_pk_add_f32 v[86:87], v[78:79], v[110:111]
	v_pk_add_f32 v[78:79], v[76:77], v[108:109]
	v_cvt_pk_bf16_f32 v76, v80, v81
	v_cvt_pk_bf16_f32 v77, v82, v83
	v_pk_add_f32 v[52:53], v[52:53], v[112:113]
	v_cvt_pk_bf16_f32 v78, v78, v79
	v_cvt_pk_bf16_f32 v79, v86, v87
	global_store_dwordx4 v[84:85], v[76:79], off
	v_pk_add_f32 v[40:41], v[40:41], v[104:105]
	v_pk_add_f32 v[42:43], v[42:43], v[106:107]
	v_pk_add_f32 v[76:77], v[70:71], v[102:103]
	v_pk_add_f32 v[70:71], v[68:69], v[100:101]
	v_cvt_pk_bf16_f32 v68, v72, v73
	v_cvt_pk_bf16_f32 v69, v74, v75
	v_pk_add_f32 v[36:37], v[36:37], v[112:113]
	v_cvt_pk_bf16_f32 v70, v70, v71
	v_cvt_pk_bf16_f32 v71, v76, v77
	global_store_dwordx4 v[84:85], v[68:71], off offset:256
	v_pk_add_f32 v[24:25], v[24:25], v[104:105]
	v_pk_add_f32 v[26:27], v[26:27], v[106:107]
	v_add_u32_e32 v68, s6, v165
	v_ashrrev_i32_e32 v69, 31, v68
	v_lshlrev_b64 v[68:69], 11, v[68:69]
	v_lshl_add_u64 v[68:69], s[10:11], 0, v[68:69]
	v_lshl_add_u64 v[68:69], v[68:69], 0, v[158:159]
	v_pk_add_f32 v[70:71], v[62:63], v[110:111]
	v_pk_add_f32 v[62:63], v[60:61], v[108:109]
	v_cvt_pk_bf16_f32 v60, v64, v65
	v_cvt_pk_bf16_f32 v61, v66, v67
	v_pk_add_f32 v[20:21], v[20:21], v[112:113]
	v_cvt_pk_bf16_f32 v62, v62, v63
	v_cvt_pk_bf16_f32 v63, v70, v71
	global_store_dwordx4 v[68:69], v[60:63], off
	v_pk_add_f32 v[10:11], v[10:11], v[106:107]
	v_pk_add_f32 v[8:9], v[8:9], v[104:105]
	v_pk_add_f32 v[60:61], v[50:51], v[102:103]
	v_pk_add_f32 v[50:51], v[48:49], v[100:101]
	v_cvt_pk_bf16_f32 v48, v56, v57
	v_cvt_pk_bf16_f32 v49, v58, v59
	s_nop 0
	v_cvt_pk_bf16_f32 v50, v50, v51
	v_cvt_pk_bf16_f32 v51, v60, v61
	global_store_dwordx4 v[68:69], v[48:51], off offset:256
	s_nop 1
	v_add_u32_e32 v48, s6, v166
	v_ashrrev_i32_e32 v49, 31, v48
	v_lshlrev_b64 v[48:49], 11, v[48:49]
	v_lshl_add_u64 v[48:49], s[10:11], 0, v[48:49]
	v_lshl_add_u64 v[48:49], v[48:49], 0, v[158:159]
	v_pk_add_f32 v[50:51], v[54:55], v[114:115]
	v_pk_add_f32 v[54:55], v[46:47], v[110:111]
	v_pk_add_f32 v[46:47], v[44:45], v[108:109]
	v_cvt_pk_bf16_f32 v44, v52, v53
	v_cvt_pk_bf16_f32 v45, v50, v51
	s_nop 0
	v_cvt_pk_bf16_f32 v46, v46, v47
	v_cvt_pk_bf16_f32 v47, v54, v55
	global_store_dwordx4 v[48:49], v[44:47], off
	s_nop 1
	v_pk_add_f32 v[44:45], v[34:35], v[102:103]
	v_pk_add_f32 v[34:35], v[32:33], v[100:101]
	v_cvt_pk_bf16_f32 v32, v40, v41
	v_cvt_pk_bf16_f32 v33, v42, v43
	s_nop 0
	v_cvt_pk_bf16_f32 v34, v34, v35
	v_cvt_pk_bf16_f32 v35, v44, v45
	global_store_dwordx4 v[48:49], v[32:35], off offset:256
	s_nop 1
	v_add_u32_e32 v32, s6, v167
	v_ashrrev_i32_e32 v33, 31, v32
	v_lshlrev_b64 v[32:33], 11, v[32:33]
	v_lshl_add_u64 v[32:33], s[10:11], 0, v[32:33]
	v_lshl_add_u64 v[32:33], v[32:33], 0, v[158:159]
	v_pk_add_f32 v[34:35], v[38:39], v[114:115]
	v_pk_add_f32 v[38:39], v[30:31], v[110:111]
	v_pk_add_f32 v[30:31], v[28:29], v[108:109]
	v_cvt_pk_bf16_f32 v28, v36, v37
	v_cvt_pk_bf16_f32 v29, v34, v35
	s_nop 0
	v_cvt_pk_bf16_f32 v30, v30, v31
	v_cvt_pk_bf16_f32 v31, v38, v39
	global_store_dwordx4 v[32:33], v[28:31], off
	s_nop 1
	v_pk_add_f32 v[28:29], v[18:19], v[102:103]
	v_pk_add_f32 v[18:19], v[16:17], v[100:101]
	v_cvt_pk_bf16_f32 v16, v24, v25
	v_cvt_pk_bf16_f32 v17, v26, v27
	s_nop 0
	v_cvt_pk_bf16_f32 v18, v18, v19
	v_cvt_pk_bf16_f32 v19, v28, v29
	global_store_dwordx4 v[32:33], v[16:19], off offset:256
	s_nop 1
	v_add_u32_e32 v16, s6, v168
	v_ashrrev_i32_e32 v17, 31, v16
	v_lshlrev_b64 v[16:17], 11, v[16:17]
	v_lshl_add_u64 v[16:17], s[10:11], 0, v[16:17]
	v_lshl_add_u64 v[16:17], v[16:17], 0, v[158:159]
	v_pk_add_f32 v[18:19], v[22:23], v[114:115]
	v_pk_add_f32 v[22:23], v[14:15], v[110:111]
	v_pk_add_f32 v[14:15], v[12:13], v[108:109]
	v_cvt_pk_bf16_f32 v12, v20, v21
	v_cvt_pk_bf16_f32 v13, v18, v19
	s_nop 0
	v_cvt_pk_bf16_f32 v14, v14, v15
	v_cvt_pk_bf16_f32 v15, v22, v23
	global_store_dwordx4 v[16:17], v[12:15], off
	s_nop 1
	v_pk_add_f32 v[12:13], v[6:7], v[102:103]
	v_pk_add_f32 v[6:7], v[4:5], v[100:101]
	v_cvt_pk_bf16_f32 v4, v8, v9
	v_cvt_pk_bf16_f32 v5, v10, v11
	s_nop 0
	v_cvt_pk_bf16_f32 v6, v6, v7
	v_cvt_pk_bf16_f32 v7, v12, v13
	global_store_dwordx4 v[16:17], v[4:7], off offset:256
	s_cbranch_vccnz .LBB0_1812
	s_branch .LBB0_1811
